# GEMM K-loops: removed the back-to-back s_setprio 0 / s_setprio 1 pair between the two 16-MFMA clusters of each segment (static priority strategy, step 1)
# baseline (speedup 1.0000x reference)
.LBB0_121:
	s_add_u32 s38, s12, 0x80
	s_addc_u32 s39, s13, 0
	s_waitcnt vmcnt(8)
	s_and_b64 s[14:15], s[14:15], exec
	s_waitcnt lgkmcnt(0)
	s_cselect_b32 s14, s57, s58
	s_cselect_b32 s41, s31, s39
	s_cselect_b32 s40, s30, s38
	s_cselect_b32 s15, s7, s59
	s_add_u32 s38, s14, 0x8000
	s_addc_u32 s39, s15, 0
	s_barrier
	s_setprio 1
	s_waitcnt lgkmcnt(0)
	v_mfma_f32_16x16x32_bf16 v[64:67], v[104:107], v[128:131], v[64:67]
	v_mfma_f32_16x16x32_bf16 v[60:63], v[112:115], v[128:131], v[60:63]
	v_mfma_f32_16x16x32_bf16 v[56:59], v[104:107], v[120:123], v[56:59]
	v_mfma_f32_16x16x32_bf16 v[52:55], v[112:115], v[120:123], v[52:55]
	v_mfma_f32_16x16x32_bf16 v[40:43], v[104:107], v[96:99], v[40:43]
	v_mfma_f32_16x16x32_bf16 v[36:39], v[112:115], v[96:99], v[36:39]
	v_mfma_f32_16x16x32_bf16 v[24:27], v[104:107], v[88:91], v[24:27]
	v_mfma_f32_16x16x32_bf16 v[20:23], v[112:115], v[88:91], v[20:23]
	v_mfma_f32_16x16x32_bf16 v[64:67], v[108:111], v[132:135], v[64:67]
	v_mfma_f32_16x16x32_bf16 v[60:63], v[116:119], v[132:135], v[60:63]
	v_mfma_f32_16x16x32_bf16 v[56:59], v[108:111], v[124:127], v[56:59]
	v_mfma_f32_16x16x32_bf16 v[52:55], v[116:119], v[124:127], v[52:55]
	v_mfma_f32_16x16x32_bf16 v[40:43], v[108:111], v[100:103], v[40:43]
	v_mfma_f32_16x16x32_bf16 v[36:39], v[116:119], v[100:103], v[36:39]
	v_mfma_f32_16x16x32_bf16 v[24:27], v[108:111], v[92:95], v[24:27]
	v_mfma_f32_16x16x32_bf16 v[20:23], v[116:119], v[92:95], v[20:23]
	v_mfma_f32_16x16x32_bf16 v[48:51], v[68:71], v[128:131], v[48:51]
	v_mfma_f32_16x16x32_bf16 v[44:47], v[76:79], v[128:131], v[44:47]
	v_mfma_f32_16x16x32_bf16 v[32:35], v[68:71], v[120:123], v[32:35]
	v_mfma_f32_16x16x32_bf16 v[28:31], v[76:79], v[120:123], v[28:31]
	v_mfma_f32_16x16x32_bf16 v[16:19], v[68:71], v[96:99], v[16:19]
	v_mfma_f32_16x16x32_bf16 v[12:15], v[76:79], v[96:99], v[12:15]
	v_mfma_f32_16x16x32_bf16 v[8:11], v[68:71], v[88:91], v[8:11]
	v_mfma_f32_16x16x32_bf16 v[4:7], v[76:79], v[88:91], v[4:7]
	v_mfma_f32_16x16x32_bf16 v[48:51], v[72:75], v[132:135], v[48:51]
	v_mfma_f32_16x16x32_bf16 v[44:47], v[80:83], v[132:135], v[44:47]
	v_mfma_f32_16x16x32_bf16 v[32:35], v[72:75], v[124:127], v[32:35]
	v_mfma_f32_16x16x32_bf16 v[28:31], v[80:83], v[124:127], v[28:31]
	v_mfma_f32_16x16x32_bf16 v[16:19], v[72:75], v[100:103], v[16:19]
	v_mfma_f32_16x16x32_bf16 v[12:15], v[80:83], v[100:103], v[12:15]
	v_mfma_f32_16x16x32_bf16 v[8:11], v[72:75], v[92:95], v[8:11]
	v_mfma_f32_16x16x32_bf16 v[4:7], v[80:83], v[92:95], v[4:7]
	s_setprio 0
	s_barrier
	s_mov_b32 m0, s43
	v_lshl_add_u64 v[68:69], s[14:15], 0, v[138:139]
	s_add_u32 s62, s14, 0x4000
	global_load_lds_dwordx4 v[68:69], off
	v_lshl_add_u64 v[68:69], s[14:15], 0, v[136:137]
	s_mov_b32 m0, s44
	s_addc_u32 s63, s15, 0
	global_load_lds_dwordx4 v[68:69], off
	v_lshl_add_u64 v[68:69], s[62:63], 0, v[138:139]
	s_mov_b32 m0, s45
	v_mov_b32_e32 v143, v3
	global_load_lds_dwordx4 v[68:69], off
	v_lshl_add_u64 v[68:69], s[62:63], 0, v[136:137]
	s_mov_b32 m0, s47
	v_lshl_add_u64 v[166:167], s[40:41], 0, v[2:3]
	global_load_lds_dwordx4 v[68:69], off
	s_mov_b32 m0, s42
	v_lshl_add_u64 v[168:169], s[40:41], 0, v[142:143]
	global_load_lds_dwordx4 v2, s[40:41]
	s_mov_b32 m0, s48
	s_nop 0
	global_load_lds_dwordx4 v142, s[40:41]
	s_waitcnt vmcnt(8)
	s_waitcnt lgkmcnt(0)
	s_barrier
	s_barrier
	s_add_i32 s61, 0, 0x18000
	s_add_i32 s62, 0, 0x1c000
	v_add_u32_e32 v80, s61, v160
	v_add_u32_e32 v100, s62, v160
	ds_read_b128 v[68:71], v80
	ds_read_b128 v[72:75], v80 offset:1024
	ds_read_b128 v[76:79], v80 offset:2048
	ds_read_b128 v[80:83], v80 offset:3072
	ds_read_b128 v[88:91], v100
	ds_read_b128 v[92:95], v100 offset:1024
	ds_read_b128 v[96:99], v100 offset:2048
	ds_read_b128 v[100:103], v100 offset:3072
	s_mov_b32 m0, s49
	v_lshl_add_u64 v[154:155], s[40:41], 0, v[154:155]
	ds_read_b128 v[104:107], v163 offset:32768
	ds_read_b128 v[108:111], v163 offset:33792
	ds_read_b128 v[112:115], v163 offset:34816
	ds_read_b128 v[116:119], v163 offset:35840
	ds_read_b128 v[120:123], v163 offset:36864
	ds_read_b128 v[124:127], v163 offset:37888
	ds_read_b128 v[128:131], v163 offset:38912
	ds_read_b128 v[132:135], v163 offset:39936
	global_load_lds_dwordx4 v[154:155], off
	v_lshl_add_u64 v[152:153], s[40:41], 0, v[152:153]
	s_mov_b32 m0, s50
	s_nop 0
	global_load_lds_dwordx4 v[152:153], off
	s_waitcnt vmcnt(8)
	s_waitcnt lgkmcnt(0)
	s_barrier
	s_setprio 1
	s_waitcnt lgkmcnt(0)
	v_mfma_f32_16x16x32_bf16 v[64:67], v[68:71], v[104:107], v[64:67]
	v_mfma_f32_16x16x32_bf16 v[60:63], v[76:79], v[104:107], v[60:63]
	v_mfma_f32_16x16x32_bf16 v[56:59], v[68:71], v[112:115], v[56:59]
	v_mfma_f32_16x16x32_bf16 v[52:55], v[76:79], v[112:115], v[52:55]
	v_mfma_f32_16x16x32_bf16 v[40:43], v[68:71], v[120:123], v[40:43]
	v_mfma_f32_16x16x32_bf16 v[36:39], v[76:79], v[120:123], v[36:39]
	v_mfma_f32_16x16x32_bf16 v[24:27], v[68:71], v[128:131], v[24:27]
	v_mfma_f32_16x16x32_bf16 v[20:23], v[76:79], v[128:131], v[20:23]
	v_mfma_f32_16x16x32_bf16 v[64:67], v[72:75], v[108:111], v[64:67]
	v_mfma_f32_16x16x32_bf16 v[60:63], v[80:83], v[108:111], v[60:63]
	v_mfma_f32_16x16x32_bf16 v[56:59], v[72:75], v[116:119], v[56:59]
	v_mfma_f32_16x16x32_bf16 v[52:55], v[80:83], v[116:119], v[52:55]
	v_mfma_f32_16x16x32_bf16 v[40:43], v[72:75], v[124:127], v[40:43]
	v_mfma_f32_16x16x32_bf16 v[36:39], v[80:83], v[124:127], v[36:39]
	v_mfma_f32_16x16x32_bf16 v[24:27], v[72:75], v[132:135], v[24:27]
	v_mfma_f32_16x16x32_bf16 v[20:23], v[80:83], v[132:135], v[20:23]
	v_mfma_f32_16x16x32_bf16 v[48:51], v[88:91], v[104:107], v[48:51]
	v_mfma_f32_16x16x32_bf16 v[44:47], v[96:99], v[104:107], v[44:47]
	v_mfma_f32_16x16x32_bf16 v[32:35], v[88:91], v[112:115], v[32:35]
	v_mfma_f32_16x16x32_bf16 v[28:31], v[96:99], v[112:115], v[28:31]
	v_mfma_f32_16x16x32_bf16 v[16:19], v[88:91], v[120:123], v[16:19]
	v_mfma_f32_16x16x32_bf16 v[12:15], v[96:99], v[120:123], v[12:15]
	v_mfma_f32_16x16x32_bf16 v[8:11], v[88:91], v[128:131], v[8:11]
	v_mfma_f32_16x16x32_bf16 v[4:7], v[96:99], v[128:131], v[4:7]
	v_mfma_f32_16x16x32_bf16 v[48:51], v[92:95], v[108:111], v[48:51]
	v_mfma_f32_16x16x32_bf16 v[44:47], v[100:103], v[108:111], v[44:47]
	v_mfma_f32_16x16x32_bf16 v[32:35], v[92:95], v[116:119], v[32:35]
	v_mfma_f32_16x16x32_bf16 v[28:31], v[100:103], v[116:119], v[28:31]
	v_mfma_f32_16x16x32_bf16 v[16:19], v[92:95], v[124:127], v[16:19]
	v_mfma_f32_16x16x32_bf16 v[12:15], v[100:103], v[124:127], v[12:15]
	v_mfma_f32_16x16x32_bf16 v[8:11], v[92:95], v[132:135], v[8:11]
	v_mfma_f32_16x16x32_bf16 v[4:7], v[100:103], v[132:135], v[4:7]
	s_setprio 0
	s_barrier
	s_add_i32 s40, s61, s33
	v_lshl_add_u64 v[68:69], s[38:39], 0, v[138:139]
	s_mov_b32 m0, s40
	s_nop 0
	global_load_lds_dwordx4 v[68:69], off
	s_add_i32 m0, s40, 0x2000
	s_add_u32 s14, s14, 0xc000
	v_lshl_add_u64 v[68:69], s[38:39], 0, v[136:137]
	s_addc_u32 s15, s15, 0
	s_add_i32 s38, s62, s33
	global_load_lds_dwordx4 v[68:69], off
	v_lshl_add_u64 v[68:69], s[14:15], 0, v[138:139]
	s_mov_b32 m0, s38
	s_nop 0
	global_load_lds_dwordx4 v[68:69], off
	v_lshl_add_u64 v[68:69], s[14:15], 0, v[136:137]
	s_add_i32 m0, s38, 0x2000
	s_nop 0
	global_load_lds_dwordx4 v[68:69], off
	v_lshl_add_u64 v[68:69], v[166:167], 0, s[36:37]
	s_mov_b32 m0, s51
	s_nop 0
	global_load_lds_dwordx4 v[68:69], off
	v_lshl_add_u64 v[68:69], v[168:169], 0, s[36:37]
	s_mov_b32 m0, s52
	s_nop 0
	global_load_lds_dwordx4 v[68:69], off
	s_waitcnt vmcnt(8)
	s_waitcnt lgkmcnt(0)
	s_barrier
	s_barrier
	s_add_i32 s60, s60, 2
	s_add_u32 s58, s58, 0x10000
	s_addc_u32 s59, s59, 0
	s_add_u32 s12, s12, 0x100
	s_addc_u32 s13, s13, 0
	s_cmp_gt_u32 s60, 29
	s_cbranch_scc1 .LBB0_124

.LBB0_144:
	s_add_u32 s40, s14, 0x80
	s_addc_u32 s41, s15, 0
	s_waitcnt vmcnt(8)
	s_and_b64 s[38:39], s[38:39], exec
	s_waitcnt lgkmcnt(0)
	s_cselect_b32 s38, s13, s60
	s_cselect_b32 s43, s31, s41
	s_cselect_b32 s42, s30, s40
	s_cselect_b32 s39, s9, s61
	s_add_u32 s40, s38, 0x8000
	s_addc_u32 s41, s39, 0
	s_barrier
	s_setprio 1
	s_waitcnt lgkmcnt(0)
	v_mfma_f32_16x16x32_bf16 v[132:135], v[152:155], v[192:195], v[132:135]
	v_mfma_f32_16x16x32_bf16 v[128:131], v[160:163], v[192:195], v[128:131]
	v_mfma_f32_16x16x32_bf16 v[124:127], v[152:155], v[184:187], v[124:127]
	v_mfma_f32_16x16x32_bf16 v[116:119], v[160:163], v[184:187], v[116:119]
	v_mfma_f32_16x16x32_bf16 v[108:111], v[152:155], v[176:179], v[108:111]
	v_mfma_f32_16x16x32_bf16 v[100:103], v[160:163], v[176:179], v[100:103]
	v_mfma_f32_16x16x32_bf16 v[92:95], v[152:155], v[168:171], v[92:95]
	v_mfma_f32_16x16x32_bf16 v[80:83], v[160:163], v[168:171], v[80:83]
	v_mfma_f32_16x16x32_bf16 v[132:135], v[156:159], v[196:199], v[132:135]
	v_mfma_f32_16x16x32_bf16 v[128:131], v[164:167], v[196:199], v[128:131]
	v_mfma_f32_16x16x32_bf16 v[124:127], v[156:159], v[188:191], v[124:127]
	v_mfma_f32_16x16x32_bf16 v[116:119], v[164:167], v[188:191], v[116:119]
	v_mfma_f32_16x16x32_bf16 v[108:111], v[156:159], v[180:183], v[108:111]
	v_mfma_f32_16x16x32_bf16 v[100:103], v[164:167], v[180:183], v[100:103]
	v_mfma_f32_16x16x32_bf16 v[92:95], v[156:159], v[172:175], v[92:95]
	v_mfma_f32_16x16x32_bf16 v[80:83], v[164:167], v[172:175], v[80:83]
	v_mfma_f32_16x16x32_bf16 v[120:123], v[136:139], v[192:195], v[120:123]
	v_mfma_f32_16x16x32_bf16 v[112:115], v[144:147], v[192:195], v[112:115]
	v_mfma_f32_16x16x32_bf16 v[104:107], v[136:139], v[184:187], v[104:107]
	v_mfma_f32_16x16x32_bf16 v[96:99], v[144:147], v[184:187], v[96:99]
	v_mfma_f32_16x16x32_bf16 v[88:91], v[136:139], v[176:179], v[88:91]
	v_mfma_f32_16x16x32_bf16 v[76:79], v[144:147], v[176:179], v[76:79]
	v_mfma_f32_16x16x32_bf16 v[72:75], v[136:139], v[168:171], v[72:75]
	v_mfma_f32_16x16x32_bf16 v[68:71], v[144:147], v[168:171], v[68:71]
	v_mfma_f32_16x16x32_bf16 v[120:123], v[140:143], v[196:199], v[120:123]
	v_mfma_f32_16x16x32_bf16 v[112:115], v[148:151], v[196:199], v[112:115]
	v_mfma_f32_16x16x32_bf16 v[104:107], v[140:143], v[188:191], v[104:107]
	v_mfma_f32_16x16x32_bf16 v[96:99], v[148:151], v[188:191], v[96:99]
	v_mfma_f32_16x16x32_bf16 v[88:91], v[140:143], v[180:183], v[88:91]
	v_mfma_f32_16x16x32_bf16 v[76:79], v[148:151], v[180:183], v[76:79]
	v_mfma_f32_16x16x32_bf16 v[72:75], v[140:143], v[172:175], v[72:75]
	v_mfma_f32_16x16x32_bf16 v[68:71], v[148:151], v[172:175], v[68:71]
	s_setprio 0
	s_barrier
	s_mov_b32 m0, s48
	v_lshl_add_u64 v[204:205], s[38:39], 0, v[210:211]
	s_add_u32 s64, s38, 0x4000
	ds_read_b128 v[168:171], v244 offset:16384
	ds_read_b128 v[172:175], v244 offset:17408
	ds_read_b128 v[176:179], v244 offset:18432
	ds_read_b128 v[180:183], v244 offset:19456
	ds_read_b128 v[184:187], v244 offset:20480
	ds_read_b128 v[188:191], v244 offset:21504
	ds_read_b128 v[192:195], v244 offset:22528
	ds_read_b128 v[196:199], v244 offset:23552
	global_load_lds_dwordx4 v[204:205], off
	v_lshl_add_u64 v[204:205], s[38:39], 0, v[208:209]
	s_mov_b32 m0, s49
	s_addc_u32 s65, s39, 0
	global_load_lds_dwordx4 v[204:205], off
	v_lshl_add_u64 v[204:205], s[64:65], 0, v[210:211]
	s_mov_b32 m0, s50
	v_mov_b32_e32 v215, v3
	global_load_lds_dwordx4 v[204:205], off
	v_lshl_add_u64 v[204:205], s[64:65], 0, v[208:209]
	s_mov_b32 m0, s51
	v_lshl_add_u64 v[248:249], s[42:43], 0, v[214:215]
	global_load_lds_dwordx4 v[204:205], off
	s_mov_b32 m0, s47
	v_lshl_add_u64 v[204:205], s[42:43], 0, v[2:3]
	global_load_lds_dwordx4 v2, s[42:43]
	s_mov_b32 m0, s52
	s_nop 0
	global_load_lds_dwordx4 v214, s[42:43]
	s_waitcnt vmcnt(8)
	s_waitcnt lgkmcnt(0)
	s_barrier
	s_setprio 1
	s_waitcnt lgkmcnt(0)
	v_mfma_f32_16x16x32_bf16 v[64:67], v[152:155], v[168:171], v[64:67]
	v_mfma_f32_16x16x32_bf16 v[60:63], v[160:163], v[168:171], v[60:63]
	v_mfma_f32_16x16x32_bf16 v[56:59], v[152:155], v[176:179], v[56:59]
	v_mfma_f32_16x16x32_bf16 v[48:51], v[160:163], v[176:179], v[48:51]
	v_mfma_f32_16x16x32_bf16 v[40:43], v[152:155], v[184:187], v[40:43]
	v_mfma_f32_16x16x32_bf16 v[32:35], v[160:163], v[184:187], v[32:35]
	v_mfma_f32_16x16x32_bf16 v[24:27], v[152:155], v[192:195], v[24:27]
	v_mfma_f32_16x16x32_bf16 v[16:19], v[160:163], v[192:195], v[16:19]
	v_mfma_f32_16x16x32_bf16 v[64:67], v[156:159], v[172:175], v[64:67]
	v_mfma_f32_16x16x32_bf16 v[60:63], v[164:167], v[172:175], v[60:63]
	v_mfma_f32_16x16x32_bf16 v[56:59], v[156:159], v[180:183], v[56:59]
	v_mfma_f32_16x16x32_bf16 v[48:51], v[164:167], v[180:183], v[48:51]
	v_mfma_f32_16x16x32_bf16 v[40:43], v[156:159], v[188:191], v[40:43]
	v_mfma_f32_16x16x32_bf16 v[32:35], v[164:167], v[188:191], v[32:35]
	v_mfma_f32_16x16x32_bf16 v[24:27], v[156:159], v[196:199], v[24:27]
	v_mfma_f32_16x16x32_bf16 v[16:19], v[164:167], v[196:199], v[16:19]
	v_mfma_f32_16x16x32_bf16 v[52:55], v[136:139], v[168:171], v[52:55]
	v_mfma_f32_16x16x32_bf16 v[44:47], v[144:147], v[168:171], v[44:47]
	v_mfma_f32_16x16x32_bf16 v[36:39], v[136:139], v[176:179], v[36:39]
	v_mfma_f32_16x16x32_bf16 v[28:31], v[144:147], v[176:179], v[28:31]
	v_mfma_f32_16x16x32_bf16 v[20:23], v[136:139], v[184:187], v[20:23]
	v_mfma_f32_16x16x32_bf16 v[12:15], v[144:147], v[184:187], v[12:15]
	v_mfma_f32_16x16x32_bf16 v[8:11], v[136:139], v[192:195], v[8:11]
	v_mfma_f32_16x16x32_bf16 v[4:7], v[144:147], v[192:195], v[4:7]
	v_mfma_f32_16x16x32_bf16 v[52:55], v[140:143], v[172:175], v[52:55]
	v_mfma_f32_16x16x32_bf16 v[44:47], v[148:151], v[172:175], v[44:47]
	v_mfma_f32_16x16x32_bf16 v[36:39], v[140:143], v[180:183], v[36:39]
	v_mfma_f32_16x16x32_bf16 v[28:31], v[148:151], v[180:183], v[28:31]
	v_mfma_f32_16x16x32_bf16 v[20:23], v[140:143], v[188:191], v[20:23]
	v_mfma_f32_16x16x32_bf16 v[12:15], v[148:151], v[188:191], v[12:15]
	v_mfma_f32_16x16x32_bf16 v[8:11], v[140:143], v[196:199], v[8:11]
	v_mfma_f32_16x16x32_bf16 v[4:7], v[148:151], v[196:199], v[4:7]
	s_setprio 0
	s_barrier
	s_add_i32 s63, 0, 0x18000
	s_add_i32 s64, 0, 0x1c000
	v_add_u32_e32 v148, s63, v243
	v_add_u32_e32 v164, s64, v243
	ds_read_b128 v[136:139], v148
	ds_read_b128 v[140:143], v148 offset:1024
	ds_read_b128 v[144:147], v148 offset:2048
	ds_read_b128 v[148:151], v148 offset:3072
	ds_read_b128 v[152:155], v164
	ds_read_b128 v[156:159], v164 offset:1024
	ds_read_b128 v[160:163], v164 offset:2048
	ds_read_b128 v[164:167], v164 offset:3072
	s_mov_b32 m0, s53
	v_lshl_add_u64 v[226:227], s[42:43], 0, v[226:227]
	ds_read_b128 v[168:171], v244 offset:32768
	ds_read_b128 v[172:175], v244 offset:33792
	ds_read_b128 v[176:179], v244 offset:34816
	ds_read_b128 v[180:183], v244 offset:35840
	ds_read_b128 v[184:187], v244 offset:36864
	ds_read_b128 v[188:191], v244 offset:37888
	ds_read_b128 v[192:195], v244 offset:38912
	ds_read_b128 v[196:199], v244 offset:39936
	global_load_lds_dwordx4 v[226:227], off
	v_lshl_add_u64 v[224:225], s[42:43], 0, v[224:225]
	s_mov_b32 m0, s54
	s_nop 0
	global_load_lds_dwordx4 v[224:225], off
	s_waitcnt vmcnt(8)
	s_waitcnt lgkmcnt(0)
	s_barrier
	s_setprio 1
	s_waitcnt lgkmcnt(0)
	v_mfma_f32_16x16x32_bf16 v[132:135], v[136:139], v[168:171], v[132:135]
	v_mfma_f32_16x16x32_bf16 v[128:131], v[144:147], v[168:171], v[128:131]
	v_mfma_f32_16x16x32_bf16 v[124:127], v[136:139], v[176:179], v[124:127]
	v_mfma_f32_16x16x32_bf16 v[116:119], v[144:147], v[176:179], v[116:119]
	v_mfma_f32_16x16x32_bf16 v[108:111], v[136:139], v[184:187], v[108:111]
	v_mfma_f32_16x16x32_bf16 v[100:103], v[144:147], v[184:187], v[100:103]
	v_mfma_f32_16x16x32_bf16 v[92:95], v[136:139], v[192:195], v[92:95]
	v_mfma_f32_16x16x32_bf16 v[80:83], v[144:147], v[192:195], v[80:83]
	v_mfma_f32_16x16x32_bf16 v[132:135], v[140:143], v[172:175], v[132:135]
	v_mfma_f32_16x16x32_bf16 v[128:131], v[148:151], v[172:175], v[128:131]
	v_mfma_f32_16x16x32_bf16 v[124:127], v[140:143], v[180:183], v[124:127]
	v_mfma_f32_16x16x32_bf16 v[116:119], v[148:151], v[180:183], v[116:119]
	v_mfma_f32_16x16x32_bf16 v[108:111], v[140:143], v[188:191], v[108:111]
	v_mfma_f32_16x16x32_bf16 v[100:103], v[148:151], v[188:191], v[100:103]
	v_mfma_f32_16x16x32_bf16 v[92:95], v[140:143], v[196:199], v[92:95]
	v_mfma_f32_16x16x32_bf16 v[80:83], v[148:151], v[196:199], v[80:83]
	v_mfma_f32_16x16x32_bf16 v[120:123], v[152:155], v[168:171], v[120:123]
	v_mfma_f32_16x16x32_bf16 v[112:115], v[160:163], v[168:171], v[112:115]
	v_mfma_f32_16x16x32_bf16 v[104:107], v[152:155], v[176:179], v[104:107]
	v_mfma_f32_16x16x32_bf16 v[96:99], v[160:163], v[176:179], v[96:99]
	v_mfma_f32_16x16x32_bf16 v[88:91], v[152:155], v[184:187], v[88:91]
	v_mfma_f32_16x16x32_bf16 v[76:79], v[160:163], v[184:187], v[76:79]
	v_mfma_f32_16x16x32_bf16 v[72:75], v[152:155], v[192:195], v[72:75]
	v_mfma_f32_16x16x32_bf16 v[68:71], v[160:163], v[192:195], v[68:71]
	v_mfma_f32_16x16x32_bf16 v[120:123], v[156:159], v[172:175], v[120:123]
	v_mfma_f32_16x16x32_bf16 v[112:115], v[164:167], v[172:175], v[112:115]
	v_mfma_f32_16x16x32_bf16 v[104:107], v[156:159], v[180:183], v[104:107]
	v_mfma_f32_16x16x32_bf16 v[96:99], v[164:167], v[180:183], v[96:99]
	v_mfma_f32_16x16x32_bf16 v[88:91], v[156:159], v[188:191], v[88:91]
	v_mfma_f32_16x16x32_bf16 v[76:79], v[164:167], v[188:191], v[76:79]
	v_mfma_f32_16x16x32_bf16 v[72:75], v[156:159], v[196:199], v[72:75]
	v_mfma_f32_16x16x32_bf16 v[68:71], v[164:167], v[196:199], v[68:71]
	s_setprio 0
	s_barrier
	s_add_i32 s42, s63, s45
	v_lshl_add_u64 v[224:225], s[40:41], 0, v[210:211]
	s_mov_b32 m0, s42
	ds_read_b128 v[168:171], v244 offset:49152
	ds_read_b128 v[172:175], v244 offset:50176
	ds_read_b128 v[176:179], v244 offset:51200
	ds_read_b128 v[180:183], v244 offset:52224
	ds_read_b128 v[184:187], v244 offset:53248
	ds_read_b128 v[188:191], v244 offset:54272
	ds_read_b128 v[192:195], v244 offset:55296
	ds_read_b128 v[196:199], v244 offset:56320
	global_load_lds_dwordx4 v[224:225], off
	s_add_i32 m0, s42, 0x2000
	s_add_u32 s38, s38, 0xc000
	v_lshl_add_u64 v[224:225], s[40:41], 0, v[208:209]
	s_addc_u32 s39, s39, 0
	s_add_i32 s40, s64, s45
	global_load_lds_dwordx4 v[224:225], off
	v_lshl_add_u64 v[224:225], s[38:39], 0, v[210:211]
	s_mov_b32 m0, s40
	v_lshl_add_u64 v[204:205], v[204:205], 0, s[36:37]
	global_load_lds_dwordx4 v[224:225], off
	v_lshl_add_u64 v[224:225], s[38:39], 0, v[208:209]
	s_add_i32 m0, s40, 0x2000
	s_nop 0
	global_load_lds_dwordx4 v[224:225], off
	s_mov_b32 m0, s55
	s_nop 0
	global_load_lds_dwordx4 v[204:205], off
	v_lshl_add_u64 v[204:205], v[248:249], 0, s[36:37]
	s_mov_b32 m0, s56
	s_nop 0
	global_load_lds_dwordx4 v[204:205], off
	s_waitcnt vmcnt(8)
	s_waitcnt lgkmcnt(0)
	s_barrier
	s_setprio 1
	s_waitcnt lgkmcnt(0)
	v_mfma_f32_16x16x32_bf16 v[64:67], v[136:139], v[168:171], v[64:67]
	v_mfma_f32_16x16x32_bf16 v[60:63], v[144:147], v[168:171], v[60:63]
	v_mfma_f32_16x16x32_bf16 v[56:59], v[136:139], v[176:179], v[56:59]
	v_mfma_f32_16x16x32_bf16 v[48:51], v[144:147], v[176:179], v[48:51]
	v_mfma_f32_16x16x32_bf16 v[40:43], v[136:139], v[184:187], v[40:43]
	v_mfma_f32_16x16x32_bf16 v[32:35], v[144:147], v[184:187], v[32:35]
	v_mfma_f32_16x16x32_bf16 v[24:27], v[136:139], v[192:195], v[24:27]
	v_mfma_f32_16x16x32_bf16 v[16:19], v[144:147], v[192:195], v[16:19]
	v_mfma_f32_16x16x32_bf16 v[64:67], v[140:143], v[172:175], v[64:67]
	v_mfma_f32_16x16x32_bf16 v[60:63], v[148:151], v[172:175], v[60:63]
	v_mfma_f32_16x16x32_bf16 v[56:59], v[140:143], v[180:183], v[56:59]
	v_mfma_f32_16x16x32_bf16 v[48:51], v[148:151], v[180:183], v[48:51]
	v_mfma_f32_16x16x32_bf16 v[40:43], v[140:143], v[188:191], v[40:43]
	v_mfma_f32_16x16x32_bf16 v[32:35], v[148:151], v[188:191], v[32:35]
	v_mfma_f32_16x16x32_bf16 v[24:27], v[140:143], v[196:199], v[24:27]
	v_mfma_f32_16x16x32_bf16 v[16:19], v[148:151], v[196:199], v[16:19]
	v_mfma_f32_16x16x32_bf16 v[52:55], v[152:155], v[168:171], v[52:55]
	v_mfma_f32_16x16x32_bf16 v[44:47], v[160:163], v[168:171], v[44:47]
	v_mfma_f32_16x16x32_bf16 v[36:39], v[152:155], v[176:179], v[36:39]
	v_mfma_f32_16x16x32_bf16 v[28:31], v[160:163], v[176:179], v[28:31]
	v_mfma_f32_16x16x32_bf16 v[20:23], v[152:155], v[184:187], v[20:23]
	v_mfma_f32_16x16x32_bf16 v[12:15], v[160:163], v[184:187], v[12:15]
	v_mfma_f32_16x16x32_bf16 v[8:11], v[152:155], v[192:195], v[8:11]
	v_mfma_f32_16x16x32_bf16 v[4:7], v[160:163], v[192:195], v[4:7]
	v_mfma_f32_16x16x32_bf16 v[52:55], v[156:159], v[172:175], v[52:55]
	v_mfma_f32_16x16x32_bf16 v[44:47], v[164:167], v[172:175], v[44:47]
	v_mfma_f32_16x16x32_bf16 v[36:39], v[156:159], v[180:183], v[36:39]
	v_mfma_f32_16x16x32_bf16 v[28:31], v[164:167], v[180:183], v[28:31]
	v_mfma_f32_16x16x32_bf16 v[20:23], v[156:159], v[188:191], v[20:23]
	v_mfma_f32_16x16x32_bf16 v[12:15], v[164:167], v[188:191], v[12:15]
	v_mfma_f32_16x16x32_bf16 v[8:11], v[156:159], v[196:199], v[8:11]
	v_mfma_f32_16x16x32_bf16 v[4:7], v[164:167], v[196:199], v[4:7]
	s_setprio 0
	s_barrier
	s_add_i32 s62, s62, 2
	s_add_u32 s60, s60, 0x10000
	s_addc_u32 s61, s61, 0
	s_add_u32 s14, s14, 0x100
	s_addc_u32 s15, s15, 0
	s_cmp_gt_u32 s62, 29
	s_cbranch_scc1 .LBB0_147

.LBB0_294:
	s_add_u32 s40, s14, 0x80
	s_addc_u32 s41, s15, 0
	s_waitcnt vmcnt(8)
	s_and_b64 s[38:39], s[38:39], exec
	s_waitcnt lgkmcnt(0)
	s_cselect_b32 s38, s13, s59
	s_cselect_b32 s43, s1, s41
	s_cselect_b32 s42, s0, s40
	s_cselect_b32 s39, s9, s60
	s_add_u32 s40, s38, 0x8000
	s_addc_u32 s41, s39, 0
	s_barrier
	s_setprio 1
	s_waitcnt lgkmcnt(0)
	v_mfma_f32_16x16x32_bf16 v[132:135], v[152:155], v[192:195], v[132:135]
	v_mfma_f32_16x16x32_bf16 v[128:131], v[160:163], v[192:195], v[128:131]
	v_mfma_f32_16x16x32_bf16 v[124:127], v[152:155], v[184:187], v[124:127]
	v_mfma_f32_16x16x32_bf16 v[120:123], v[160:163], v[184:187], v[120:123]
	v_mfma_f32_16x16x32_bf16 v[108:111], v[152:155], v[176:179], v[108:111]
	v_mfma_f32_16x16x32_bf16 v[104:107], v[160:163], v[176:179], v[104:107]
	v_mfma_f32_16x16x32_bf16 v[92:95], v[152:155], v[168:171], v[92:95]
	v_mfma_f32_16x16x32_bf16 v[88:91], v[160:163], v[168:171], v[88:91]
	v_mfma_f32_16x16x32_bf16 v[132:135], v[156:159], v[196:199], v[132:135]
	v_mfma_f32_16x16x32_bf16 v[128:131], v[164:167], v[196:199], v[128:131]
	v_mfma_f32_16x16x32_bf16 v[124:127], v[156:159], v[188:191], v[124:127]
	v_mfma_f32_16x16x32_bf16 v[120:123], v[164:167], v[188:191], v[120:123]
	v_mfma_f32_16x16x32_bf16 v[108:111], v[156:159], v[180:183], v[108:111]
	v_mfma_f32_16x16x32_bf16 v[104:107], v[164:167], v[180:183], v[104:107]
	v_mfma_f32_16x16x32_bf16 v[92:95], v[156:159], v[172:175], v[92:95]
	v_mfma_f32_16x16x32_bf16 v[88:91], v[164:167], v[172:175], v[88:91]
	v_mfma_f32_16x16x32_bf16 v[116:119], v[136:139], v[192:195], v[116:119]
	v_mfma_f32_16x16x32_bf16 v[112:115], v[144:147], v[192:195], v[112:115]
	v_mfma_f32_16x16x32_bf16 v[100:103], v[136:139], v[184:187], v[100:103]
	v_mfma_f32_16x16x32_bf16 v[96:99], v[144:147], v[184:187], v[96:99]
	v_mfma_f32_16x16x32_bf16 v[80:83], v[136:139], v[176:179], v[80:83]
	v_mfma_f32_16x16x32_bf16 v[76:79], v[144:147], v[176:179], v[76:79]
	v_mfma_f32_16x16x32_bf16 v[72:75], v[136:139], v[168:171], v[72:75]
	v_mfma_f32_16x16x32_bf16 v[68:71], v[144:147], v[168:171], v[68:71]
	v_mfma_f32_16x16x32_bf16 v[116:119], v[140:143], v[196:199], v[116:119]
	v_mfma_f32_16x16x32_bf16 v[112:115], v[148:151], v[196:199], v[112:115]
	v_mfma_f32_16x16x32_bf16 v[100:103], v[140:143], v[188:191], v[100:103]
	v_mfma_f32_16x16x32_bf16 v[96:99], v[148:151], v[188:191], v[96:99]
	v_mfma_f32_16x16x32_bf16 v[80:83], v[140:143], v[180:183], v[80:83]
	v_mfma_f32_16x16x32_bf16 v[76:79], v[148:151], v[180:183], v[76:79]
	v_mfma_f32_16x16x32_bf16 v[72:75], v[140:143], v[172:175], v[72:75]
	v_mfma_f32_16x16x32_bf16 v[68:71], v[148:151], v[172:175], v[68:71]
	s_setprio 0
	s_barrier
	s_mov_b32 m0, s47
	v_lshl_add_u64 v[204:205], s[38:39], 0, v[210:211]
	s_add_u32 s62, s38, 0x4000
	ds_read_b128 v[168:171], v244 offset:16384
	ds_read_b128 v[172:175], v244 offset:17408
	ds_read_b128 v[176:179], v244 offset:18432
	ds_read_b128 v[180:183], v244 offset:19456
	ds_read_b128 v[184:187], v244 offset:20480
	ds_read_b128 v[188:191], v244 offset:21504
	ds_read_b128 v[192:195], v244 offset:22528
	ds_read_b128 v[196:199], v244 offset:23552
	global_load_lds_dwordx4 v[204:205], off
	v_lshl_add_u64 v[204:205], s[38:39], 0, v[208:209]
	s_mov_b32 m0, s48
	s_addc_u32 s63, s39, 0
	global_load_lds_dwordx4 v[204:205], off
	v_lshl_add_u64 v[204:205], s[62:63], 0, v[210:211]
	s_mov_b32 m0, s49
	v_mov_b32_e32 v215, v3
	global_load_lds_dwordx4 v[204:205], off
	v_lshl_add_u64 v[204:205], s[62:63], 0, v[208:209]
	s_mov_b32 m0, s50
	v_lshl_add_u64 v[248:249], s[42:43], 0, v[214:215]
	global_load_lds_dwordx4 v[204:205], off
	s_mov_b32 m0, s45
	v_lshl_add_u64 v[204:205], s[42:43], 0, v[2:3]
	global_load_lds_dwordx4 v2, s[42:43]
	s_mov_b32 m0, s51
	s_nop 0
	global_load_lds_dwordx4 v214, s[42:43]
	s_waitcnt vmcnt(8)
	s_waitcnt lgkmcnt(0)
	s_barrier
	s_setprio 1
	s_waitcnt lgkmcnt(0)
	v_mfma_f32_16x16x32_bf16 v[64:67], v[152:155], v[168:171], v[64:67]
	v_mfma_f32_16x16x32_bf16 v[60:63], v[160:163], v[168:171], v[60:63]
	v_mfma_f32_16x16x32_bf16 v[56:59], v[152:155], v[176:179], v[56:59]
	v_mfma_f32_16x16x32_bf16 v[52:55], v[160:163], v[176:179], v[52:55]
	v_mfma_f32_16x16x32_bf16 v[40:43], v[152:155], v[184:187], v[40:43]
	v_mfma_f32_16x16x32_bf16 v[36:39], v[160:163], v[184:187], v[36:39]
	v_mfma_f32_16x16x32_bf16 v[24:27], v[152:155], v[192:195], v[24:27]
	v_mfma_f32_16x16x32_bf16 v[20:23], v[160:163], v[192:195], v[20:23]
	v_mfma_f32_16x16x32_bf16 v[64:67], v[156:159], v[172:175], v[64:67]
	v_mfma_f32_16x16x32_bf16 v[60:63], v[164:167], v[172:175], v[60:63]
	v_mfma_f32_16x16x32_bf16 v[56:59], v[156:159], v[180:183], v[56:59]
	v_mfma_f32_16x16x32_bf16 v[52:55], v[164:167], v[180:183], v[52:55]
	v_mfma_f32_16x16x32_bf16 v[40:43], v[156:159], v[188:191], v[40:43]
	v_mfma_f32_16x16x32_bf16 v[36:39], v[164:167], v[188:191], v[36:39]
	v_mfma_f32_16x16x32_bf16 v[24:27], v[156:159], v[196:199], v[24:27]
	v_mfma_f32_16x16x32_bf16 v[20:23], v[164:167], v[196:199], v[20:23]
	v_mfma_f32_16x16x32_bf16 v[48:51], v[136:139], v[168:171], v[48:51]
	v_mfma_f32_16x16x32_bf16 v[44:47], v[144:147], v[168:171], v[44:47]
	v_mfma_f32_16x16x32_bf16 v[32:35], v[136:139], v[176:179], v[32:35]
	v_mfma_f32_16x16x32_bf16 v[28:31], v[144:147], v[176:179], v[28:31]
	v_mfma_f32_16x16x32_bf16 v[16:19], v[136:139], v[184:187], v[16:19]
	v_mfma_f32_16x16x32_bf16 v[12:15], v[144:147], v[184:187], v[12:15]
	v_mfma_f32_16x16x32_bf16 v[8:11], v[136:139], v[192:195], v[8:11]
	v_mfma_f32_16x16x32_bf16 v[4:7], v[144:147], v[192:195], v[4:7]
	v_mfma_f32_16x16x32_bf16 v[48:51], v[140:143], v[172:175], v[48:51]
	v_mfma_f32_16x16x32_bf16 v[44:47], v[148:151], v[172:175], v[44:47]
	v_mfma_f32_16x16x32_bf16 v[32:35], v[140:143], v[180:183], v[32:35]
	v_mfma_f32_16x16x32_bf16 v[28:31], v[148:151], v[180:183], v[28:31]
	v_mfma_f32_16x16x32_bf16 v[16:19], v[140:143], v[188:191], v[16:19]
	v_mfma_f32_16x16x32_bf16 v[12:15], v[148:151], v[188:191], v[12:15]
	v_mfma_f32_16x16x32_bf16 v[8:11], v[140:143], v[196:199], v[8:11]
	v_mfma_f32_16x16x32_bf16 v[4:7], v[148:151], v[196:199], v[4:7]
	s_setprio 0
	s_barrier
	s_add_i32 s62, 0, 0x18000
	s_add_i32 s63, 0, 0x1c000
	v_add_u32_e32 v148, s62, v243
	v_add_u32_e32 v164, s63, v243
	ds_read_b128 v[136:139], v148
	ds_read_b128 v[140:143], v148 offset:1024
	ds_read_b128 v[144:147], v148 offset:2048
	ds_read_b128 v[148:151], v148 offset:3072
	ds_read_b128 v[152:155], v164
	ds_read_b128 v[156:159], v164 offset:1024
	ds_read_b128 v[160:163], v164 offset:2048
	ds_read_b128 v[164:167], v164 offset:3072
	s_mov_b32 m0, s52
	v_lshl_add_u64 v[226:227], s[42:43], 0, v[226:227]
	ds_read_b128 v[168:171], v244 offset:32768
	ds_read_b128 v[172:175], v244 offset:33792
	ds_read_b128 v[176:179], v244 offset:34816
	ds_read_b128 v[180:183], v244 offset:35840
	ds_read_b128 v[184:187], v244 offset:36864
	ds_read_b128 v[188:191], v244 offset:37888
	ds_read_b128 v[192:195], v244 offset:38912
	ds_read_b128 v[196:199], v244 offset:39936
	global_load_lds_dwordx4 v[226:227], off
	v_lshl_add_u64 v[224:225], s[42:43], 0, v[224:225]
	s_mov_b32 m0, s53
	s_nop 0
	global_load_lds_dwordx4 v[224:225], off
	s_waitcnt vmcnt(8)
	s_waitcnt lgkmcnt(0)
	s_barrier
	s_setprio 1
	s_waitcnt lgkmcnt(0)
	v_mfma_f32_16x16x32_bf16 v[132:135], v[136:139], v[168:171], v[132:135]
	v_mfma_f32_16x16x32_bf16 v[128:131], v[144:147], v[168:171], v[128:131]
	v_mfma_f32_16x16x32_bf16 v[124:127], v[136:139], v[176:179], v[124:127]
	v_mfma_f32_16x16x32_bf16 v[120:123], v[144:147], v[176:179], v[120:123]
	v_mfma_f32_16x16x32_bf16 v[108:111], v[136:139], v[184:187], v[108:111]
	v_mfma_f32_16x16x32_bf16 v[104:107], v[144:147], v[184:187], v[104:107]
	v_mfma_f32_16x16x32_bf16 v[92:95], v[136:139], v[192:195], v[92:95]
	v_mfma_f32_16x16x32_bf16 v[88:91], v[144:147], v[192:195], v[88:91]
	v_mfma_f32_16x16x32_bf16 v[132:135], v[140:143], v[172:175], v[132:135]
	v_mfma_f32_16x16x32_bf16 v[128:131], v[148:151], v[172:175], v[128:131]
	v_mfma_f32_16x16x32_bf16 v[124:127], v[140:143], v[180:183], v[124:127]
	v_mfma_f32_16x16x32_bf16 v[120:123], v[148:151], v[180:183], v[120:123]
	v_mfma_f32_16x16x32_bf16 v[108:111], v[140:143], v[188:191], v[108:111]
	v_mfma_f32_16x16x32_bf16 v[104:107], v[148:151], v[188:191], v[104:107]
	v_mfma_f32_16x16x32_bf16 v[92:95], v[140:143], v[196:199], v[92:95]
	v_mfma_f32_16x16x32_bf16 v[88:91], v[148:151], v[196:199], v[88:91]
	v_mfma_f32_16x16x32_bf16 v[116:119], v[152:155], v[168:171], v[116:119]
	v_mfma_f32_16x16x32_bf16 v[112:115], v[160:163], v[168:171], v[112:115]
	v_mfma_f32_16x16x32_bf16 v[100:103], v[152:155], v[176:179], v[100:103]
	v_mfma_f32_16x16x32_bf16 v[96:99], v[160:163], v[176:179], v[96:99]
	v_mfma_f32_16x16x32_bf16 v[80:83], v[152:155], v[184:187], v[80:83]
	v_mfma_f32_16x16x32_bf16 v[76:79], v[160:163], v[184:187], v[76:79]
	v_mfma_f32_16x16x32_bf16 v[72:75], v[152:155], v[192:195], v[72:75]
	v_mfma_f32_16x16x32_bf16 v[68:71], v[160:163], v[192:195], v[68:71]
	v_mfma_f32_16x16x32_bf16 v[116:119], v[156:159], v[172:175], v[116:119]
	v_mfma_f32_16x16x32_bf16 v[112:115], v[164:167], v[172:175], v[112:115]
	v_mfma_f32_16x16x32_bf16 v[100:103], v[156:159], v[180:183], v[100:103]
	v_mfma_f32_16x16x32_bf16 v[96:99], v[164:167], v[180:183], v[96:99]
	v_mfma_f32_16x16x32_bf16 v[80:83], v[156:159], v[188:191], v[80:83]
	v_mfma_f32_16x16x32_bf16 v[76:79], v[164:167], v[188:191], v[76:79]
	v_mfma_f32_16x16x32_bf16 v[72:75], v[156:159], v[196:199], v[72:75]
	v_mfma_f32_16x16x32_bf16 v[68:71], v[164:167], v[196:199], v[68:71]
	s_setprio 0
	s_barrier
	s_add_i32 s42, s62, s44
	v_lshl_add_u64 v[224:225], s[40:41], 0, v[210:211]
	s_mov_b32 m0, s42
	ds_read_b128 v[168:171], v244 offset:49152
	ds_read_b128 v[172:175], v244 offset:50176
	ds_read_b128 v[176:179], v244 offset:51200
	ds_read_b128 v[180:183], v244 offset:52224
	ds_read_b128 v[184:187], v244 offset:53248
	ds_read_b128 v[188:191], v244 offset:54272
	ds_read_b128 v[192:195], v244 offset:55296
	ds_read_b128 v[196:199], v244 offset:56320
	global_load_lds_dwordx4 v[224:225], off
	s_add_i32 m0, s42, 0x2000
	s_add_u32 s38, s38, 0xc000
	v_lshl_add_u64 v[224:225], s[40:41], 0, v[208:209]
	s_addc_u32 s39, s39, 0
	s_add_i32 s40, s63, s44
	global_load_lds_dwordx4 v[224:225], off
	v_lshl_add_u64 v[224:225], s[38:39], 0, v[210:211]
	s_mov_b32 m0, s40
	v_lshl_add_u64 v[204:205], v[204:205], 0, s[36:37]
	global_load_lds_dwordx4 v[224:225], off
	v_lshl_add_u64 v[224:225], s[38:39], 0, v[208:209]
	s_add_i32 m0, s40, 0x2000
	s_nop 0
	global_load_lds_dwordx4 v[224:225], off
	s_mov_b32 m0, s54
	s_nop 0
	global_load_lds_dwordx4 v[204:205], off
	v_lshl_add_u64 v[204:205], v[248:249], 0, s[36:37]
	s_mov_b32 m0, s55
	s_nop 0
	global_load_lds_dwordx4 v[204:205], off
	s_waitcnt vmcnt(8)
	s_waitcnt lgkmcnt(0)
	s_barrier
	s_setprio 1
	s_waitcnt lgkmcnt(0)
	v_mfma_f32_16x16x32_bf16 v[64:67], v[136:139], v[168:171], v[64:67]
	v_mfma_f32_16x16x32_bf16 v[60:63], v[144:147], v[168:171], v[60:63]
	v_mfma_f32_16x16x32_bf16 v[56:59], v[136:139], v[176:179], v[56:59]
	v_mfma_f32_16x16x32_bf16 v[52:55], v[144:147], v[176:179], v[52:55]
	v_mfma_f32_16x16x32_bf16 v[40:43], v[136:139], v[184:187], v[40:43]
	v_mfma_f32_16x16x32_bf16 v[36:39], v[144:147], v[184:187], v[36:39]
	v_mfma_f32_16x16x32_bf16 v[24:27], v[136:139], v[192:195], v[24:27]
	v_mfma_f32_16x16x32_bf16 v[20:23], v[144:147], v[192:195], v[20:23]
	v_mfma_f32_16x16x32_bf16 v[64:67], v[140:143], v[172:175], v[64:67]
	v_mfma_f32_16x16x32_bf16 v[60:63], v[148:151], v[172:175], v[60:63]
	v_mfma_f32_16x16x32_bf16 v[56:59], v[140:143], v[180:183], v[56:59]
	v_mfma_f32_16x16x32_bf16 v[52:55], v[148:151], v[180:183], v[52:55]
	v_mfma_f32_16x16x32_bf16 v[40:43], v[140:143], v[188:191], v[40:43]
	v_mfma_f32_16x16x32_bf16 v[36:39], v[148:151], v[188:191], v[36:39]
	v_mfma_f32_16x16x32_bf16 v[24:27], v[140:143], v[196:199], v[24:27]
	v_mfma_f32_16x16x32_bf16 v[20:23], v[148:151], v[196:199], v[20:23]
	v_mfma_f32_16x16x32_bf16 v[48:51], v[152:155], v[168:171], v[48:51]
	v_mfma_f32_16x16x32_bf16 v[44:47], v[160:163], v[168:171], v[44:47]
	v_mfma_f32_16x16x32_bf16 v[32:35], v[152:155], v[176:179], v[32:35]
	v_mfma_f32_16x16x32_bf16 v[28:31], v[160:163], v[176:179], v[28:31]
	v_mfma_f32_16x16x32_bf16 v[16:19], v[152:155], v[184:187], v[16:19]
	v_mfma_f32_16x16x32_bf16 v[12:15], v[160:163], v[184:187], v[12:15]
	v_mfma_f32_16x16x32_bf16 v[8:11], v[152:155], v[192:195], v[8:11]
	v_mfma_f32_16x16x32_bf16 v[4:7], v[160:163], v[192:195], v[4:7]
	v_mfma_f32_16x16x32_bf16 v[48:51], v[156:159], v[172:175], v[48:51]
	v_mfma_f32_16x16x32_bf16 v[44:47], v[164:167], v[172:175], v[44:47]
	v_mfma_f32_16x16x32_bf16 v[32:35], v[156:159], v[180:183], v[32:35]
	v_mfma_f32_16x16x32_bf16 v[28:31], v[164:167], v[180:183], v[28:31]
	v_mfma_f32_16x16x32_bf16 v[16:19], v[156:159], v[188:191], v[16:19]
	v_mfma_f32_16x16x32_bf16 v[12:15], v[164:167], v[188:191], v[12:15]
	v_mfma_f32_16x16x32_bf16 v[8:11], v[156:159], v[196:199], v[8:11]
	v_mfma_f32_16x16x32_bf16 v[4:7], v[164:167], v[196:199], v[4:7]
	s_setprio 0
	s_barrier
	s_add_i32 s61, s61, 2
	s_add_u32 s59, s59, 0x10000
	s_addc_u32 s60, s60, 0
	s_add_u32 s14, s14, 0x100
	s_addc_u32 s15, s15, 0
	s_cmp_gt_u32 s61, 29
	s_cbranch_scc1 .LBB0_297

.LBB0_498:
	s_add_u32 s38, s12, 0x80
	s_addc_u32 s39, s13, 0
	s_waitcnt vmcnt(8)
	s_and_b64 s[14:15], s[14:15], exec
	s_waitcnt lgkmcnt(0)
	s_cselect_b32 s14, s60, s61
	s_cselect_b32 s41, s31, s39
	s_cselect_b32 s40, s30, s38
	s_cselect_b32 s15, s9, s62
	s_add_u32 s38, s14, 0x8000
	s_addc_u32 s39, s15, 0
	s_barrier
	s_setprio 1
	s_waitcnt lgkmcnt(0)
	v_mfma_f32_16x16x32_bf16 v[132:135], v[152:155], v[192:195], v[132:135]
	v_mfma_f32_16x16x32_bf16 v[128:131], v[160:163], v[192:195], v[128:131]
	v_mfma_f32_16x16x32_bf16 v[124:127], v[152:155], v[184:187], v[124:127]
	v_mfma_f32_16x16x32_bf16 v[120:123], v[160:163], v[184:187], v[120:123]
	v_mfma_f32_16x16x32_bf16 v[108:111], v[152:155], v[176:179], v[108:111]
	v_mfma_f32_16x16x32_bf16 v[104:107], v[160:163], v[176:179], v[104:107]
	v_mfma_f32_16x16x32_bf16 v[92:95], v[152:155], v[168:171], v[92:95]
	v_mfma_f32_16x16x32_bf16 v[88:91], v[160:163], v[168:171], v[88:91]
	v_mfma_f32_16x16x32_bf16 v[132:135], v[156:159], v[196:199], v[132:135]
	v_mfma_f32_16x16x32_bf16 v[128:131], v[164:167], v[196:199], v[128:131]
	v_mfma_f32_16x16x32_bf16 v[124:127], v[156:159], v[188:191], v[124:127]
	v_mfma_f32_16x16x32_bf16 v[120:123], v[164:167], v[188:191], v[120:123]
	v_mfma_f32_16x16x32_bf16 v[108:111], v[156:159], v[180:183], v[108:111]
	v_mfma_f32_16x16x32_bf16 v[104:107], v[164:167], v[180:183], v[104:107]
	v_mfma_f32_16x16x32_bf16 v[92:95], v[156:159], v[172:175], v[92:95]
	v_mfma_f32_16x16x32_bf16 v[88:91], v[164:167], v[172:175], v[88:91]
	v_mfma_f32_16x16x32_bf16 v[116:119], v[136:139], v[192:195], v[116:119]
	v_mfma_f32_16x16x32_bf16 v[112:115], v[144:147], v[192:195], v[112:115]
	v_mfma_f32_16x16x32_bf16 v[100:103], v[136:139], v[184:187], v[100:103]
	v_mfma_f32_16x16x32_bf16 v[96:99], v[144:147], v[184:187], v[96:99]
	v_mfma_f32_16x16x32_bf16 v[80:83], v[136:139], v[176:179], v[80:83]
	v_mfma_f32_16x16x32_bf16 v[76:79], v[144:147], v[176:179], v[76:79]
	v_mfma_f32_16x16x32_bf16 v[72:75], v[136:139], v[168:171], v[72:75]
	v_mfma_f32_16x16x32_bf16 v[68:71], v[144:147], v[168:171], v[68:71]
	v_mfma_f32_16x16x32_bf16 v[116:119], v[140:143], v[196:199], v[116:119]
	v_mfma_f32_16x16x32_bf16 v[112:115], v[148:151], v[196:199], v[112:115]
	v_mfma_f32_16x16x32_bf16 v[100:103], v[140:143], v[188:191], v[100:103]
	v_mfma_f32_16x16x32_bf16 v[96:99], v[148:151], v[188:191], v[96:99]
	v_mfma_f32_16x16x32_bf16 v[80:83], v[140:143], v[180:183], v[80:83]
	v_mfma_f32_16x16x32_bf16 v[76:79], v[148:151], v[180:183], v[76:79]
	v_mfma_f32_16x16x32_bf16 v[72:75], v[140:143], v[172:175], v[72:75]
	v_mfma_f32_16x16x32_bf16 v[68:71], v[148:151], v[172:175], v[68:71]
	s_setprio 0
	s_barrier
	s_mov_b32 m0, s44
	v_lshl_add_u64 v[246:247], s[14:15], 0, v[210:211]
	s_add_u32 s64, s14, 0x4000
	ds_read_b128 v[168:171], v243 offset:16384
	ds_read_b128 v[172:175], v243 offset:17408
	ds_read_b128 v[176:179], v243 offset:18432
	ds_read_b128 v[180:183], v243 offset:19456
	ds_read_b128 v[184:187], v243 offset:20480
	ds_read_b128 v[188:191], v243 offset:21504
	ds_read_b128 v[192:195], v243 offset:22528
	ds_read_b128 v[196:199], v243 offset:23552
	global_load_lds_dwordx4 v[246:247], off
	v_lshl_add_u64 v[246:247], s[14:15], 0, v[208:209]
	s_mov_b32 m0, s45
	s_addc_u32 s65, s15, 0
	global_load_lds_dwordx4 v[246:247], off
	v_lshl_add_u64 v[246:247], s[64:65], 0, v[210:211]
	s_mov_b32 m0, s47
	v_mov_b32_e32 v215, v3
	global_load_lds_dwordx4 v[246:247], off
	v_lshl_add_u64 v[246:247], s[64:65], 0, v[208:209]
	s_mov_b32 m0, s48
	v_lshl_add_u64 v[248:249], s[40:41], 0, v[214:215]
	global_load_lds_dwordx4 v[246:247], off
	s_mov_b32 m0, s43
	v_lshl_add_u64 v[246:247], s[40:41], 0, v[2:3]
	global_load_lds_dwordx4 v2, s[40:41]
	s_mov_b32 m0, s49
	s_nop 0
	global_load_lds_dwordx4 v214, s[40:41]
	s_waitcnt vmcnt(8)
	s_waitcnt lgkmcnt(0)
	s_barrier
	s_setprio 1
	s_waitcnt lgkmcnt(0)
	v_mfma_f32_16x16x32_bf16 v[64:67], v[152:155], v[168:171], v[64:67]
	v_mfma_f32_16x16x32_bf16 v[60:63], v[160:163], v[168:171], v[60:63]
	v_mfma_f32_16x16x32_bf16 v[56:59], v[152:155], v[176:179], v[56:59]
	v_mfma_f32_16x16x32_bf16 v[52:55], v[160:163], v[176:179], v[52:55]
	v_mfma_f32_16x16x32_bf16 v[40:43], v[152:155], v[184:187], v[40:43]
	v_mfma_f32_16x16x32_bf16 v[36:39], v[160:163], v[184:187], v[36:39]
	v_mfma_f32_16x16x32_bf16 v[24:27], v[152:155], v[192:195], v[24:27]
	v_mfma_f32_16x16x32_bf16 v[20:23], v[160:163], v[192:195], v[20:23]
	v_mfma_f32_16x16x32_bf16 v[64:67], v[156:159], v[172:175], v[64:67]
	v_mfma_f32_16x16x32_bf16 v[60:63], v[164:167], v[172:175], v[60:63]
	v_mfma_f32_16x16x32_bf16 v[56:59], v[156:159], v[180:183], v[56:59]
	v_mfma_f32_16x16x32_bf16 v[52:55], v[164:167], v[180:183], v[52:55]
	v_mfma_f32_16x16x32_bf16 v[40:43], v[156:159], v[188:191], v[40:43]
	v_mfma_f32_16x16x32_bf16 v[36:39], v[164:167], v[188:191], v[36:39]
	v_mfma_f32_16x16x32_bf16 v[24:27], v[156:159], v[196:199], v[24:27]
	v_mfma_f32_16x16x32_bf16 v[20:23], v[164:167], v[196:199], v[20:23]
	v_mfma_f32_16x16x32_bf16 v[48:51], v[136:139], v[168:171], v[48:51]
	v_mfma_f32_16x16x32_bf16 v[44:47], v[144:147], v[168:171], v[44:47]
	v_mfma_f32_16x16x32_bf16 v[32:35], v[136:139], v[176:179], v[32:35]
	v_mfma_f32_16x16x32_bf16 v[28:31], v[144:147], v[176:179], v[28:31]
	v_mfma_f32_16x16x32_bf16 v[16:19], v[136:139], v[184:187], v[16:19]
	v_mfma_f32_16x16x32_bf16 v[12:15], v[144:147], v[184:187], v[12:15]
	v_mfma_f32_16x16x32_bf16 v[8:11], v[136:139], v[192:195], v[8:11]
	v_mfma_f32_16x16x32_bf16 v[4:7], v[144:147], v[192:195], v[4:7]
	v_mfma_f32_16x16x32_bf16 v[48:51], v[140:143], v[172:175], v[48:51]
	v_mfma_f32_16x16x32_bf16 v[44:47], v[148:151], v[172:175], v[44:47]
	v_mfma_f32_16x16x32_bf16 v[32:35], v[140:143], v[180:183], v[32:35]
	v_mfma_f32_16x16x32_bf16 v[28:31], v[148:151], v[180:183], v[28:31]
	v_mfma_f32_16x16x32_bf16 v[16:19], v[140:143], v[188:191], v[16:19]
	v_mfma_f32_16x16x32_bf16 v[12:15], v[148:151], v[188:191], v[12:15]
	v_mfma_f32_16x16x32_bf16 v[8:11], v[140:143], v[196:199], v[8:11]
	v_mfma_f32_16x16x32_bf16 v[4:7], v[148:151], v[196:199], v[4:7]
	s_setprio 0
	s_barrier
	s_add_i32 s64, 0, 0x18000
	s_add_i32 s65, 0, 0x1c000
	v_add_u32_e32 v148, s64, v241
	v_add_u32_e32 v164, s65, v241
	ds_read_b128 v[136:139], v148
	ds_read_b128 v[140:143], v148 offset:1024
	ds_read_b128 v[144:147], v148 offset:2048
	ds_read_b128 v[148:151], v148 offset:3072
	ds_read_b128 v[152:155], v164
	ds_read_b128 v[156:159], v164 offset:1024
	ds_read_b128 v[160:163], v164 offset:2048
	ds_read_b128 v[164:167], v164 offset:3072
	s_mov_b32 m0, s50
	v_lshl_add_u64 v[224:225], s[40:41], 0, v[224:225]
	ds_read_b128 v[168:171], v243 offset:32768
	ds_read_b128 v[172:175], v243 offset:33792
	ds_read_b128 v[176:179], v243 offset:34816
	ds_read_b128 v[180:183], v243 offset:35840
	ds_read_b128 v[184:187], v243 offset:36864
	ds_read_b128 v[188:191], v243 offset:37888
	ds_read_b128 v[192:195], v243 offset:38912
	ds_read_b128 v[196:199], v243 offset:39936
	global_load_lds_dwordx4 v[224:225], off
	v_lshl_add_u64 v[222:223], s[40:41], 0, v[222:223]
	s_mov_b32 m0, s51
	s_nop 0
	global_load_lds_dwordx4 v[222:223], off
	s_waitcnt vmcnt(8)
	s_waitcnt lgkmcnt(0)
	s_barrier
	s_setprio 1
	s_waitcnt lgkmcnt(0)
	v_mfma_f32_16x16x32_bf16 v[132:135], v[136:139], v[168:171], v[132:135]
	v_mfma_f32_16x16x32_bf16 v[128:131], v[144:147], v[168:171], v[128:131]
	v_mfma_f32_16x16x32_bf16 v[124:127], v[136:139], v[176:179], v[124:127]
	v_mfma_f32_16x16x32_bf16 v[120:123], v[144:147], v[176:179], v[120:123]
	v_mfma_f32_16x16x32_bf16 v[108:111], v[136:139], v[184:187], v[108:111]
	v_mfma_f32_16x16x32_bf16 v[104:107], v[144:147], v[184:187], v[104:107]
	v_mfma_f32_16x16x32_bf16 v[92:95], v[136:139], v[192:195], v[92:95]
	v_mfma_f32_16x16x32_bf16 v[88:91], v[144:147], v[192:195], v[88:91]
	v_mfma_f32_16x16x32_bf16 v[132:135], v[140:143], v[172:175], v[132:135]
	v_mfma_f32_16x16x32_bf16 v[128:131], v[148:151], v[172:175], v[128:131]
	v_mfma_f32_16x16x32_bf16 v[124:127], v[140:143], v[180:183], v[124:127]
	v_mfma_f32_16x16x32_bf16 v[120:123], v[148:151], v[180:183], v[120:123]
	v_mfma_f32_16x16x32_bf16 v[108:111], v[140:143], v[188:191], v[108:111]
	v_mfma_f32_16x16x32_bf16 v[104:107], v[148:151], v[188:191], v[104:107]
	v_mfma_f32_16x16x32_bf16 v[92:95], v[140:143], v[196:199], v[92:95]
	v_mfma_f32_16x16x32_bf16 v[88:91], v[148:151], v[196:199], v[88:91]
	v_mfma_f32_16x16x32_bf16 v[116:119], v[152:155], v[168:171], v[116:119]
	v_mfma_f32_16x16x32_bf16 v[112:115], v[160:163], v[168:171], v[112:115]
	v_mfma_f32_16x16x32_bf16 v[100:103], v[152:155], v[176:179], v[100:103]
	v_mfma_f32_16x16x32_bf16 v[96:99], v[160:163], v[176:179], v[96:99]
	v_mfma_f32_16x16x32_bf16 v[80:83], v[152:155], v[184:187], v[80:83]
	v_mfma_f32_16x16x32_bf16 v[76:79], v[160:163], v[184:187], v[76:79]
	v_mfma_f32_16x16x32_bf16 v[72:75], v[152:155], v[192:195], v[72:75]
	v_mfma_f32_16x16x32_bf16 v[68:71], v[160:163], v[192:195], v[68:71]
	v_mfma_f32_16x16x32_bf16 v[116:119], v[156:159], v[172:175], v[116:119]
	v_mfma_f32_16x16x32_bf16 v[112:115], v[164:167], v[172:175], v[112:115]
	v_mfma_f32_16x16x32_bf16 v[100:103], v[156:159], v[180:183], v[100:103]
	v_mfma_f32_16x16x32_bf16 v[96:99], v[164:167], v[180:183], v[96:99]
	v_mfma_f32_16x16x32_bf16 v[80:83], v[156:159], v[188:191], v[80:83]
	v_mfma_f32_16x16x32_bf16 v[76:79], v[164:167], v[188:191], v[76:79]
	v_mfma_f32_16x16x32_bf16 v[72:75], v[156:159], v[196:199], v[72:75]
	v_mfma_f32_16x16x32_bf16 v[68:71], v[164:167], v[196:199], v[68:71]
	s_setprio 0
	s_barrier
	s_add_i32 s40, s64, s42
	v_lshl_add_u64 v[222:223], s[38:39], 0, v[210:211]
	s_mov_b32 m0, s40
	ds_read_b128 v[168:171], v243 offset:49152
	ds_read_b128 v[172:175], v243 offset:50176
	ds_read_b128 v[176:179], v243 offset:51200
	ds_read_b128 v[180:183], v243 offset:52224
	ds_read_b128 v[184:187], v243 offset:53248
	ds_read_b128 v[188:191], v243 offset:54272
	ds_read_b128 v[192:195], v243 offset:55296
	ds_read_b128 v[196:199], v243 offset:56320
	global_load_lds_dwordx4 v[222:223], off
	s_add_i32 m0, s40, 0x2000
	s_add_u32 s14, s14, 0xc000
	v_lshl_add_u64 v[222:223], s[38:39], 0, v[208:209]
	s_addc_u32 s15, s15, 0
	s_add_i32 s38, s65, s42
	global_load_lds_dwordx4 v[222:223], off
	v_lshl_add_u64 v[222:223], s[14:15], 0, v[210:211]
	s_mov_b32 m0, s38
	s_nop 0
	global_load_lds_dwordx4 v[222:223], off
	v_lshl_add_u64 v[222:223], s[14:15], 0, v[208:209]
	s_add_i32 m0, s38, 0x2000
	s_nop 0
	global_load_lds_dwordx4 v[222:223], off
	v_lshl_add_u64 v[222:223], v[246:247], 0, s[36:37]
	s_mov_b32 m0, s53
	s_nop 0
	global_load_lds_dwordx4 v[222:223], off
	v_lshl_add_u64 v[222:223], v[248:249], 0, s[36:37]
	s_mov_b32 m0, s54
	s_nop 0
	global_load_lds_dwordx4 v[222:223], off
	s_waitcnt vmcnt(8)
	s_waitcnt lgkmcnt(0)
	s_barrier
	s_setprio 1
	s_waitcnt lgkmcnt(0)
	v_mfma_f32_16x16x32_bf16 v[64:67], v[136:139], v[168:171], v[64:67]
	v_mfma_f32_16x16x32_bf16 v[60:63], v[144:147], v[168:171], v[60:63]
	v_mfma_f32_16x16x32_bf16 v[56:59], v[136:139], v[176:179], v[56:59]
	v_mfma_f32_16x16x32_bf16 v[52:55], v[144:147], v[176:179], v[52:55]
	v_mfma_f32_16x16x32_bf16 v[40:43], v[136:139], v[184:187], v[40:43]
	v_mfma_f32_16x16x32_bf16 v[36:39], v[144:147], v[184:187], v[36:39]
	v_mfma_f32_16x16x32_bf16 v[24:27], v[136:139], v[192:195], v[24:27]
	v_mfma_f32_16x16x32_bf16 v[20:23], v[144:147], v[192:195], v[20:23]
	v_mfma_f32_16x16x32_bf16 v[64:67], v[140:143], v[172:175], v[64:67]
	v_mfma_f32_16x16x32_bf16 v[60:63], v[148:151], v[172:175], v[60:63]
	v_mfma_f32_16x16x32_bf16 v[56:59], v[140:143], v[180:183], v[56:59]
	v_mfma_f32_16x16x32_bf16 v[52:55], v[148:151], v[180:183], v[52:55]
	v_mfma_f32_16x16x32_bf16 v[40:43], v[140:143], v[188:191], v[40:43]
	v_mfma_f32_16x16x32_bf16 v[36:39], v[148:151], v[188:191], v[36:39]
	v_mfma_f32_16x16x32_bf16 v[24:27], v[140:143], v[196:199], v[24:27]
	v_mfma_f32_16x16x32_bf16 v[20:23], v[148:151], v[196:199], v[20:23]
	v_mfma_f32_16x16x32_bf16 v[48:51], v[152:155], v[168:171], v[48:51]
	v_mfma_f32_16x16x32_bf16 v[44:47], v[160:163], v[168:171], v[44:47]
	v_mfma_f32_16x16x32_bf16 v[32:35], v[152:155], v[176:179], v[32:35]
	v_mfma_f32_16x16x32_bf16 v[28:31], v[160:163], v[176:179], v[28:31]
	v_mfma_f32_16x16x32_bf16 v[16:19], v[152:155], v[184:187], v[16:19]
	v_mfma_f32_16x16x32_bf16 v[12:15], v[160:163], v[184:187], v[12:15]
	v_mfma_f32_16x16x32_bf16 v[8:11], v[152:155], v[192:195], v[8:11]
	v_mfma_f32_16x16x32_bf16 v[4:7], v[160:163], v[192:195], v[4:7]
	v_mfma_f32_16x16x32_bf16 v[48:51], v[156:159], v[172:175], v[48:51]
	v_mfma_f32_16x16x32_bf16 v[44:47], v[164:167], v[172:175], v[44:47]
	v_mfma_f32_16x16x32_bf16 v[32:35], v[156:159], v[180:183], v[32:35]
	v_mfma_f32_16x16x32_bf16 v[28:31], v[164:167], v[180:183], v[28:31]
	v_mfma_f32_16x16x32_bf16 v[16:19], v[156:159], v[188:191], v[16:19]
	v_mfma_f32_16x16x32_bf16 v[12:15], v[164:167], v[188:191], v[12:15]
	v_mfma_f32_16x16x32_bf16 v[8:11], v[156:159], v[196:199], v[8:11]
	v_mfma_f32_16x16x32_bf16 v[4:7], v[164:167], v[196:199], v[4:7]
	s_setprio 0
	s_barrier
	s_add_i32 s63, s63, 2
	s_add_u32 s61, s61, 0x10000
	s_addc_u32 s62, s62, 0
	s_add_u32 s12, s12, 0x100
	s_addc_u32 s13, s13, 0
	s_cmp_gt_u32 s63, 29
	s_cbranch_scc1 .LBB0_501

.LBB0_835:
	s_add_u32 s40, s14, 0x80
	s_addc_u32 s41, s15, 0
	s_waitcnt vmcnt(8)
	s_and_b64 s[38:39], s[38:39], exec
	s_waitcnt lgkmcnt(0)
	s_cselect_b32 s38, s13, s59
	s_cselect_b32 s43, s1, s41
	s_cselect_b32 s42, s0, s40
	s_cselect_b32 s39, s9, s60
	s_add_u32 s40, s38, 0x8000
	s_addc_u32 s41, s39, 0
	s_barrier
	s_setprio 1
	s_waitcnt lgkmcnt(0)
	v_mfma_f32_16x16x32_bf16 v[132:135], v[152:155], v[192:195], v[132:135]
	v_mfma_f32_16x16x32_bf16 v[128:131], v[160:163], v[192:195], v[128:131]
	v_mfma_f32_16x16x32_bf16 v[124:127], v[152:155], v[184:187], v[124:127]
	v_mfma_f32_16x16x32_bf16 v[120:123], v[160:163], v[184:187], v[120:123]
	v_mfma_f32_16x16x32_bf16 v[108:111], v[152:155], v[176:179], v[108:111]
	v_mfma_f32_16x16x32_bf16 v[104:107], v[160:163], v[176:179], v[104:107]
	v_mfma_f32_16x16x32_bf16 v[92:95], v[152:155], v[168:171], v[92:95]
	v_mfma_f32_16x16x32_bf16 v[88:91], v[160:163], v[168:171], v[88:91]
	v_mfma_f32_16x16x32_bf16 v[132:135], v[156:159], v[196:199], v[132:135]
	v_mfma_f32_16x16x32_bf16 v[128:131], v[164:167], v[196:199], v[128:131]
	v_mfma_f32_16x16x32_bf16 v[124:127], v[156:159], v[188:191], v[124:127]
	v_mfma_f32_16x16x32_bf16 v[120:123], v[164:167], v[188:191], v[120:123]
	v_mfma_f32_16x16x32_bf16 v[108:111], v[156:159], v[180:183], v[108:111]
	v_mfma_f32_16x16x32_bf16 v[104:107], v[164:167], v[180:183], v[104:107]
	v_mfma_f32_16x16x32_bf16 v[92:95], v[156:159], v[172:175], v[92:95]
	v_mfma_f32_16x16x32_bf16 v[88:91], v[164:167], v[172:175], v[88:91]
	v_mfma_f32_16x16x32_bf16 v[116:119], v[136:139], v[192:195], v[116:119]
	v_mfma_f32_16x16x32_bf16 v[112:115], v[144:147], v[192:195], v[112:115]
	v_mfma_f32_16x16x32_bf16 v[100:103], v[136:139], v[184:187], v[100:103]
	v_mfma_f32_16x16x32_bf16 v[96:99], v[144:147], v[184:187], v[96:99]
	v_mfma_f32_16x16x32_bf16 v[80:83], v[136:139], v[176:179], v[80:83]
	v_mfma_f32_16x16x32_bf16 v[76:79], v[144:147], v[176:179], v[76:79]
	v_mfma_f32_16x16x32_bf16 v[72:75], v[136:139], v[168:171], v[72:75]
	v_mfma_f32_16x16x32_bf16 v[68:71], v[144:147], v[168:171], v[68:71]
	v_mfma_f32_16x16x32_bf16 v[116:119], v[140:143], v[196:199], v[116:119]
	v_mfma_f32_16x16x32_bf16 v[112:115], v[148:151], v[196:199], v[112:115]
	v_mfma_f32_16x16x32_bf16 v[100:103], v[140:143], v[188:191], v[100:103]
	v_mfma_f32_16x16x32_bf16 v[96:99], v[148:151], v[188:191], v[96:99]
	v_mfma_f32_16x16x32_bf16 v[80:83], v[140:143], v[180:183], v[80:83]
	v_mfma_f32_16x16x32_bf16 v[76:79], v[148:151], v[180:183], v[76:79]
	v_mfma_f32_16x16x32_bf16 v[72:75], v[140:143], v[172:175], v[72:75]
	v_mfma_f32_16x16x32_bf16 v[68:71], v[148:151], v[172:175], v[68:71]
	s_setprio 0
	s_barrier
	s_mov_b32 m0, s47
	v_lshl_add_u64 v[248:249], s[38:39], 0, v[210:211]
	s_add_u32 s62, s38, 0x4000
	ds_read_b128 v[168:171], v244 offset:16384
	ds_read_b128 v[172:175], v244 offset:17408
	ds_read_b128 v[176:179], v244 offset:18432
	ds_read_b128 v[180:183], v244 offset:19456
	ds_read_b128 v[184:187], v244 offset:20480
	ds_read_b128 v[188:191], v244 offset:21504
	ds_read_b128 v[192:195], v244 offset:22528
	ds_read_b128 v[196:199], v244 offset:23552
	global_load_lds_dwordx4 v[248:249], off
	v_lshl_add_u64 v[248:249], s[38:39], 0, v[208:209]
	s_mov_b32 m0, s48
	s_addc_u32 s63, s39, 0
	global_load_lds_dwordx4 v[248:249], off
	v_lshl_add_u64 v[248:249], s[62:63], 0, v[210:211]
	s_mov_b32 m0, s49
	v_mov_b32_e32 v215, v3
	global_load_lds_dwordx4 v[248:249], off
	v_lshl_add_u64 v[248:249], s[62:63], 0, v[208:209]
	s_mov_b32 m0, s50
	v_lshl_add_u64 v[204:205], s[42:43], 0, v[214:215]
	global_load_lds_dwordx4 v[248:249], off
	s_mov_b32 m0, s45
	v_lshl_add_u64 v[248:249], s[42:43], 0, v[2:3]
	global_load_lds_dwordx4 v2, s[42:43]
	s_mov_b32 m0, s51
	s_nop 0
	global_load_lds_dwordx4 v214, s[42:43]
	s_waitcnt vmcnt(8)
	s_waitcnt lgkmcnt(0)
	s_barrier
	s_setprio 1
	s_waitcnt lgkmcnt(0)
	v_mfma_f32_16x16x32_bf16 v[64:67], v[152:155], v[168:171], v[64:67]
	v_mfma_f32_16x16x32_bf16 v[60:63], v[160:163], v[168:171], v[60:63]
	v_mfma_f32_16x16x32_bf16 v[56:59], v[152:155], v[176:179], v[56:59]
	v_mfma_f32_16x16x32_bf16 v[52:55], v[160:163], v[176:179], v[52:55]
	v_mfma_f32_16x16x32_bf16 v[40:43], v[152:155], v[184:187], v[40:43]
	v_mfma_f32_16x16x32_bf16 v[36:39], v[160:163], v[184:187], v[36:39]
	v_mfma_f32_16x16x32_bf16 v[24:27], v[152:155], v[192:195], v[24:27]
	v_mfma_f32_16x16x32_bf16 v[20:23], v[160:163], v[192:195], v[20:23]
	v_mfma_f32_16x16x32_bf16 v[64:67], v[156:159], v[172:175], v[64:67]
	v_mfma_f32_16x16x32_bf16 v[60:63], v[164:167], v[172:175], v[60:63]
	v_mfma_f32_16x16x32_bf16 v[56:59], v[156:159], v[180:183], v[56:59]
	v_mfma_f32_16x16x32_bf16 v[52:55], v[164:167], v[180:183], v[52:55]
	v_mfma_f32_16x16x32_bf16 v[40:43], v[156:159], v[188:191], v[40:43]
	v_mfma_f32_16x16x32_bf16 v[36:39], v[164:167], v[188:191], v[36:39]
	v_mfma_f32_16x16x32_bf16 v[24:27], v[156:159], v[196:199], v[24:27]
	v_mfma_f32_16x16x32_bf16 v[20:23], v[164:167], v[196:199], v[20:23]
	v_mfma_f32_16x16x32_bf16 v[48:51], v[136:139], v[168:171], v[48:51]
	v_mfma_f32_16x16x32_bf16 v[44:47], v[144:147], v[168:171], v[44:47]
	v_mfma_f32_16x16x32_bf16 v[32:35], v[136:139], v[176:179], v[32:35]
	v_mfma_f32_16x16x32_bf16 v[28:31], v[144:147], v[176:179], v[28:31]
	v_mfma_f32_16x16x32_bf16 v[16:19], v[136:139], v[184:187], v[16:19]
	v_mfma_f32_16x16x32_bf16 v[12:15], v[144:147], v[184:187], v[12:15]
	v_mfma_f32_16x16x32_bf16 v[8:11], v[136:139], v[192:195], v[8:11]
	v_mfma_f32_16x16x32_bf16 v[4:7], v[144:147], v[192:195], v[4:7]
	v_mfma_f32_16x16x32_bf16 v[48:51], v[140:143], v[172:175], v[48:51]
	v_mfma_f32_16x16x32_bf16 v[44:47], v[148:151], v[172:175], v[44:47]
	v_mfma_f32_16x16x32_bf16 v[32:35], v[140:143], v[180:183], v[32:35]
	v_mfma_f32_16x16x32_bf16 v[28:31], v[148:151], v[180:183], v[28:31]
	v_mfma_f32_16x16x32_bf16 v[16:19], v[140:143], v[188:191], v[16:19]
	v_mfma_f32_16x16x32_bf16 v[12:15], v[148:151], v[188:191], v[12:15]
	v_mfma_f32_16x16x32_bf16 v[8:11], v[140:143], v[196:199], v[8:11]
	v_mfma_f32_16x16x32_bf16 v[4:7], v[148:151], v[196:199], v[4:7]
	s_setprio 0
	s_barrier
	s_add_i32 s62, 0, 0x18000
	s_add_i32 s63, 0, 0x1c000
	v_add_u32_e32 v148, s62, v243
	v_add_u32_e32 v164, s63, v243
	ds_read_b128 v[136:139], v148
	ds_read_b128 v[140:143], v148 offset:1024
	ds_read_b128 v[144:147], v148 offset:2048
	ds_read_b128 v[148:151], v148 offset:3072
	ds_read_b128 v[152:155], v164
	ds_read_b128 v[156:159], v164 offset:1024
	ds_read_b128 v[160:163], v164 offset:2048
	ds_read_b128 v[164:167], v164 offset:3072
	s_mov_b32 m0, s52
	v_lshl_add_u64 v[226:227], s[42:43], 0, v[226:227]
	ds_read_b128 v[168:171], v244 offset:32768
	ds_read_b128 v[172:175], v244 offset:33792
	ds_read_b128 v[176:179], v244 offset:34816
	ds_read_b128 v[180:183], v244 offset:35840
	ds_read_b128 v[184:187], v244 offset:36864
	ds_read_b128 v[188:191], v244 offset:37888
	ds_read_b128 v[192:195], v244 offset:38912
	ds_read_b128 v[196:199], v244 offset:39936
	global_load_lds_dwordx4 v[226:227], off
	v_lshl_add_u64 v[224:225], s[42:43], 0, v[224:225]
	s_mov_b32 m0, s53
	s_nop 0
	global_load_lds_dwordx4 v[224:225], off
	s_waitcnt vmcnt(8)
	s_waitcnt lgkmcnt(0)
	s_barrier
	s_setprio 1
	s_waitcnt lgkmcnt(0)
	v_mfma_f32_16x16x32_bf16 v[132:135], v[136:139], v[168:171], v[132:135]
	v_mfma_f32_16x16x32_bf16 v[128:131], v[144:147], v[168:171], v[128:131]
	v_mfma_f32_16x16x32_bf16 v[124:127], v[136:139], v[176:179], v[124:127]
	v_mfma_f32_16x16x32_bf16 v[120:123], v[144:147], v[176:179], v[120:123]
	v_mfma_f32_16x16x32_bf16 v[108:111], v[136:139], v[184:187], v[108:111]
	v_mfma_f32_16x16x32_bf16 v[104:107], v[144:147], v[184:187], v[104:107]
	v_mfma_f32_16x16x32_bf16 v[92:95], v[136:139], v[192:195], v[92:95]
	v_mfma_f32_16x16x32_bf16 v[88:91], v[144:147], v[192:195], v[88:91]
	v_mfma_f32_16x16x32_bf16 v[132:135], v[140:143], v[172:175], v[132:135]
	v_mfma_f32_16x16x32_bf16 v[128:131], v[148:151], v[172:175], v[128:131]
	v_mfma_f32_16x16x32_bf16 v[124:127], v[140:143], v[180:183], v[124:127]
	v_mfma_f32_16x16x32_bf16 v[120:123], v[148:151], v[180:183], v[120:123]
	v_mfma_f32_16x16x32_bf16 v[108:111], v[140:143], v[188:191], v[108:111]
	v_mfma_f32_16x16x32_bf16 v[104:107], v[148:151], v[188:191], v[104:107]
	v_mfma_f32_16x16x32_bf16 v[92:95], v[140:143], v[196:199], v[92:95]
	v_mfma_f32_16x16x32_bf16 v[88:91], v[148:151], v[196:199], v[88:91]
	v_mfma_f32_16x16x32_bf16 v[116:119], v[152:155], v[168:171], v[116:119]
	v_mfma_f32_16x16x32_bf16 v[112:115], v[160:163], v[168:171], v[112:115]
	v_mfma_f32_16x16x32_bf16 v[100:103], v[152:155], v[176:179], v[100:103]
	v_mfma_f32_16x16x32_bf16 v[96:99], v[160:163], v[176:179], v[96:99]
	v_mfma_f32_16x16x32_bf16 v[80:83], v[152:155], v[184:187], v[80:83]
	v_mfma_f32_16x16x32_bf16 v[76:79], v[160:163], v[184:187], v[76:79]
	v_mfma_f32_16x16x32_bf16 v[72:75], v[152:155], v[192:195], v[72:75]
	v_mfma_f32_16x16x32_bf16 v[68:71], v[160:163], v[192:195], v[68:71]
	v_mfma_f32_16x16x32_bf16 v[116:119], v[156:159], v[172:175], v[116:119]
	v_mfma_f32_16x16x32_bf16 v[112:115], v[164:167], v[172:175], v[112:115]
	v_mfma_f32_16x16x32_bf16 v[100:103], v[156:159], v[180:183], v[100:103]
	v_mfma_f32_16x16x32_bf16 v[96:99], v[164:167], v[180:183], v[96:99]
	v_mfma_f32_16x16x32_bf16 v[80:83], v[156:159], v[188:191], v[80:83]
	v_mfma_f32_16x16x32_bf16 v[76:79], v[164:167], v[188:191], v[76:79]
	v_mfma_f32_16x16x32_bf16 v[72:75], v[156:159], v[196:199], v[72:75]
	v_mfma_f32_16x16x32_bf16 v[68:71], v[164:167], v[196:199], v[68:71]
	s_setprio 0
	s_barrier
	s_add_i32 s42, s62, s44
	v_lshl_add_u64 v[224:225], s[40:41], 0, v[210:211]
	s_mov_b32 m0, s42
	ds_read_b128 v[168:171], v244 offset:49152
	ds_read_b128 v[172:175], v244 offset:50176
	ds_read_b128 v[176:179], v244 offset:51200
	ds_read_b128 v[180:183], v244 offset:52224
	ds_read_b128 v[184:187], v244 offset:53248
	ds_read_b128 v[188:191], v244 offset:54272
	ds_read_b128 v[192:195], v244 offset:55296
	ds_read_b128 v[196:199], v244 offset:56320
	global_load_lds_dwordx4 v[224:225], off
	s_add_i32 m0, s42, 0x2000
	s_add_u32 s38, s38, 0xc000
	v_lshl_add_u64 v[224:225], s[40:41], 0, v[208:209]
	s_addc_u32 s39, s39, 0
	s_add_i32 s40, s63, s44
	global_load_lds_dwordx4 v[224:225], off
	v_lshl_add_u64 v[224:225], s[38:39], 0, v[210:211]
	s_mov_b32 m0, s40
	v_lshl_add_u64 v[204:205], v[204:205], 0, s[36:37]
	global_load_lds_dwordx4 v[224:225], off
	v_lshl_add_u64 v[224:225], s[38:39], 0, v[208:209]
	s_add_i32 m0, s40, 0x2000
	s_nop 0
	global_load_lds_dwordx4 v[224:225], off
	v_lshl_add_u64 v[224:225], v[248:249], 0, s[36:37]
	s_mov_b32 m0, s54
	s_nop 0
	global_load_lds_dwordx4 v[224:225], off
	s_mov_b32 m0, s55
	s_nop 0
	global_load_lds_dwordx4 v[204:205], off
	s_waitcnt vmcnt(8)
	s_waitcnt lgkmcnt(0)
	s_barrier
	s_setprio 1
	s_waitcnt lgkmcnt(0)
	v_mfma_f32_16x16x32_bf16 v[64:67], v[136:139], v[168:171], v[64:67]
	v_mfma_f32_16x16x32_bf16 v[60:63], v[144:147], v[168:171], v[60:63]
	v_mfma_f32_16x16x32_bf16 v[56:59], v[136:139], v[176:179], v[56:59]
	v_mfma_f32_16x16x32_bf16 v[52:55], v[144:147], v[176:179], v[52:55]
	v_mfma_f32_16x16x32_bf16 v[40:43], v[136:139], v[184:187], v[40:43]
	v_mfma_f32_16x16x32_bf16 v[36:39], v[144:147], v[184:187], v[36:39]
	v_mfma_f32_16x16x32_bf16 v[24:27], v[136:139], v[192:195], v[24:27]
	v_mfma_f32_16x16x32_bf16 v[20:23], v[144:147], v[192:195], v[20:23]
	v_mfma_f32_16x16x32_bf16 v[64:67], v[140:143], v[172:175], v[64:67]
	v_mfma_f32_16x16x32_bf16 v[60:63], v[148:151], v[172:175], v[60:63]
	v_mfma_f32_16x16x32_bf16 v[56:59], v[140:143], v[180:183], v[56:59]
	v_mfma_f32_16x16x32_bf16 v[52:55], v[148:151], v[180:183], v[52:55]
	v_mfma_f32_16x16x32_bf16 v[40:43], v[140:143], v[188:191], v[40:43]
	v_mfma_f32_16x16x32_bf16 v[36:39], v[148:151], v[188:191], v[36:39]
	v_mfma_f32_16x16x32_bf16 v[24:27], v[140:143], v[196:199], v[24:27]
	v_mfma_f32_16x16x32_bf16 v[20:23], v[148:151], v[196:199], v[20:23]
	v_mfma_f32_16x16x32_bf16 v[48:51], v[152:155], v[168:171], v[48:51]
	v_mfma_f32_16x16x32_bf16 v[44:47], v[160:163], v[168:171], v[44:47]
	v_mfma_f32_16x16x32_bf16 v[32:35], v[152:155], v[176:179], v[32:35]
	v_mfma_f32_16x16x32_bf16 v[28:31], v[160:163], v[176:179], v[28:31]
	v_mfma_f32_16x16x32_bf16 v[16:19], v[152:155], v[184:187], v[16:19]
	v_mfma_f32_16x16x32_bf16 v[12:15], v[160:163], v[184:187], v[12:15]
	v_mfma_f32_16x16x32_bf16 v[8:11], v[152:155], v[192:195], v[8:11]
	v_mfma_f32_16x16x32_bf16 v[4:7], v[160:163], v[192:195], v[4:7]
	v_mfma_f32_16x16x32_bf16 v[48:51], v[156:159], v[172:175], v[48:51]
	v_mfma_f32_16x16x32_bf16 v[44:47], v[164:167], v[172:175], v[44:47]
	v_mfma_f32_16x16x32_bf16 v[32:35], v[156:159], v[180:183], v[32:35]
	v_mfma_f32_16x16x32_bf16 v[28:31], v[164:167], v[180:183], v[28:31]
	v_mfma_f32_16x16x32_bf16 v[16:19], v[156:159], v[188:191], v[16:19]
	v_mfma_f32_16x16x32_bf16 v[12:15], v[164:167], v[188:191], v[12:15]
	v_mfma_f32_16x16x32_bf16 v[8:11], v[156:159], v[196:199], v[8:11]
	v_mfma_f32_16x16x32_bf16 v[4:7], v[164:167], v[196:199], v[4:7]
	s_setprio 0
	s_barrier
	s_add_i32 s61, s61, 2
	s_add_u32 s59, s59, 0x10000
	s_addc_u32 s60, s60, 0
	s_add_u32 s14, s14, 0x100
	s_addc_u32 s15, s15, 0
	s_cmp_gt_u32 s61, 29
	s_cbranch_scc1 .LBB0_838

.LBB0_1175:
	s_waitcnt vmcnt(8)
	s_waitcnt lgkmcnt(0)
	s_barrier
	s_setprio 1
	s_waitcnt lgkmcnt(0)
	v_mfma_f32_16x16x32_bf16 v[132:135], v[152:155], v[180:183], v[132:135]
	v_mfma_f32_16x16x32_bf16 v[128:131], v[160:163], v[180:183], v[128:131]
	v_mfma_f32_16x16x32_bf16 v[124:127], v[152:155], v[176:179], v[124:127]
	v_mfma_f32_16x16x32_bf16 v[120:123], v[160:163], v[176:179], v[120:123]
	v_mfma_f32_16x16x32_bf16 v[116:119], v[152:155], v[172:175], v[116:119]
	v_mfma_f32_16x16x32_bf16 v[112:115], v[160:163], v[172:175], v[112:115]
	v_mfma_f32_16x16x32_bf16 v[108:111], v[152:155], v[168:171], v[108:111]
	v_mfma_f32_16x16x32_bf16 v[104:107], v[160:163], v[168:171], v[104:107]
	v_mfma_f32_16x16x32_bf16 v[132:135], v[156:159], v[196:199], v[132:135]
	v_mfma_f32_16x16x32_bf16 v[128:131], v[164:167], v[196:199], v[128:131]
	v_mfma_f32_16x16x32_bf16 v[124:127], v[156:159], v[192:195], v[124:127]
	v_mfma_f32_16x16x32_bf16 v[120:123], v[164:167], v[192:195], v[120:123]
	v_mfma_f32_16x16x32_bf16 v[116:119], v[156:159], v[188:191], v[116:119]
	v_mfma_f32_16x16x32_bf16 v[112:115], v[164:167], v[188:191], v[112:115]
	v_mfma_f32_16x16x32_bf16 v[108:111], v[156:159], v[184:187], v[108:111]
	v_mfma_f32_16x16x32_bf16 v[104:107], v[164:167], v[184:187], v[104:107]
	v_mfma_f32_16x16x32_bf16 v[100:103], v[136:139], v[180:183], v[100:103]
	v_mfma_f32_16x16x32_bf16 v[96:99], v[144:147], v[180:183], v[96:99]
	v_mfma_f32_16x16x32_bf16 v[92:95], v[136:139], v[176:179], v[92:95]
	v_mfma_f32_16x16x32_bf16 v[88:91], v[144:147], v[176:179], v[88:91]
	v_mfma_f32_16x16x32_bf16 v[80:83], v[136:139], v[172:175], v[80:83]
	v_mfma_f32_16x16x32_bf16 v[76:79], v[144:147], v[172:175], v[76:79]
	v_mfma_f32_16x16x32_bf16 v[72:75], v[136:139], v[168:171], v[72:75]
	v_mfma_f32_16x16x32_bf16 v[68:71], v[144:147], v[168:171], v[68:71]
	v_mfma_f32_16x16x32_bf16 v[100:103], v[140:143], v[196:199], v[100:103]
	v_mfma_f32_16x16x32_bf16 v[96:99], v[148:151], v[196:199], v[96:99]
	v_mfma_f32_16x16x32_bf16 v[92:95], v[140:143], v[192:195], v[92:95]
	v_mfma_f32_16x16x32_bf16 v[88:91], v[148:151], v[192:195], v[88:91]
	v_mfma_f32_16x16x32_bf16 v[80:83], v[140:143], v[188:191], v[80:83]
	v_mfma_f32_16x16x32_bf16 v[76:79], v[148:151], v[188:191], v[76:79]
	v_mfma_f32_16x16x32_bf16 v[72:75], v[140:143], v[184:187], v[72:75]
	v_mfma_f32_16x16x32_bf16 v[68:71], v[148:151], v[184:187], v[68:71]
	s_setprio 0
	s_barrier
	v_cndmask_b32_e64 v200, 0, 1, s[2:3]
	v_cmp_ne_u32_e64 s[4:5], 1, v200
	s_andn2_b64 vcc, exec, s[2:3]
	s_cbranch_vccnz .LBB0_1177
	ds_read_b128 v[180:183], v225 offset:16384
	ds_read_b128 v[196:199], v225 offset:17408
	ds_read_b128 v[176:179], v225 offset:18432
	ds_read_b128 v[192:195], v225 offset:19456
	ds_read_b128 v[172:175], v225 offset:20480
	ds_read_b128 v[188:191], v225 offset:21504
	ds_read_b128 v[168:171], v225 offset:22528
	ds_read_b128 v[184:187], v225 offset:23552
.LBB0_1177:
	s_add_u32 s56, s52, 0x80
	s_addc_u32 s57, s53, 0
	s_and_b64 s[54:55], s[54:55], exec
	s_cselect_b32 s55, s11, s81
	s_cselect_b32 s54, s41, s80
	s_mov_b32 m0, s61
	s_cselect_b32 s57, s23, s57
	s_cselect_b32 s56, s22, s56
	v_lshl_add_u64 v[204:205], s[54:55], 0, v[208:209]
	s_add_u32 s84, s54, 0x4000
	global_load_lds_dwordx4 v[204:205], off
	v_lshl_add_u64 v[204:205], s[54:55], 0, v[210:211]
	s_mov_b32 m0, s62
	s_addc_u32 s85, s55, 0
	global_load_lds_dwordx4 v[204:205], off
	v_lshl_add_u64 v[204:205], s[84:85], 0, v[208:209]
	s_mov_b32 m0, s63
	s_and_b64 vcc, exec, s[4:5]
	global_load_lds_dwordx4 v[204:205], off
	v_lshl_add_u64 v[204:205], s[84:85], 0, v[210:211]
	s_mov_b32 m0, s64
	s_nop 0
	global_load_lds_dwordx4 v[204:205], off
	s_mov_b32 m0, s9
	s_nop 0
	global_load_lds_dwordx4 v2, s[56:57]
	s_mov_b32 m0, s65
	s_nop 0
	global_load_lds_dwordx4 v212, s[56:57]
	s_waitcnt vmcnt(8)
	s_waitcnt lgkmcnt(0)
	s_barrier
	s_cbranch_vccnz .LBB0_1179
	s_setprio 1
	s_waitcnt lgkmcnt(0)
	v_mfma_f32_16x16x32_bf16 v[64:67], v[152:155], v[180:183], v[64:67]
	v_mfma_f32_16x16x32_bf16 v[60:63], v[160:163], v[180:183], v[60:63]
	v_mfma_f32_16x16x32_bf16 v[56:59], v[152:155], v[176:179], v[56:59]
	v_mfma_f32_16x16x32_bf16 v[52:55], v[160:163], v[176:179], v[52:55]
	v_mfma_f32_16x16x32_bf16 v[48:51], v[152:155], v[172:175], v[48:51]
	v_mfma_f32_16x16x32_bf16 v[44:47], v[160:163], v[172:175], v[44:47]
	v_mfma_f32_16x16x32_bf16 v[40:43], v[152:155], v[168:171], v[40:43]
	v_mfma_f32_16x16x32_bf16 v[36:39], v[160:163], v[168:171], v[36:39]
	v_mfma_f32_16x16x32_bf16 v[64:67], v[156:159], v[196:199], v[64:67]
	v_mfma_f32_16x16x32_bf16 v[60:63], v[164:167], v[196:199], v[60:63]
	v_mfma_f32_16x16x32_bf16 v[56:59], v[156:159], v[192:195], v[56:59]
	v_mfma_f32_16x16x32_bf16 v[52:55], v[164:167], v[192:195], v[52:55]
	v_mfma_f32_16x16x32_bf16 v[48:51], v[156:159], v[188:191], v[48:51]
	v_mfma_f32_16x16x32_bf16 v[44:47], v[164:167], v[188:191], v[44:47]
	v_mfma_f32_16x16x32_bf16 v[40:43], v[156:159], v[184:187], v[40:43]
	v_mfma_f32_16x16x32_bf16 v[36:39], v[164:167], v[184:187], v[36:39]
	v_mfma_f32_16x16x32_bf16 v[32:35], v[136:139], v[180:183], v[32:35]
	v_mfma_f32_16x16x32_bf16 v[28:31], v[144:147], v[180:183], v[28:31]
	v_mfma_f32_16x16x32_bf16 v[24:27], v[136:139], v[176:179], v[24:27]
	v_mfma_f32_16x16x32_bf16 v[20:23], v[144:147], v[176:179], v[20:23]
	v_mfma_f32_16x16x32_bf16 v[16:19], v[136:139], v[172:175], v[16:19]
	v_mfma_f32_16x16x32_bf16 v[12:15], v[144:147], v[172:175], v[12:15]
	v_mfma_f32_16x16x32_bf16 v[8:11], v[136:139], v[168:171], v[8:11]
	v_mfma_f32_16x16x32_bf16 v[4:7], v[144:147], v[168:171], v[4:7]
	v_mfma_f32_16x16x32_bf16 v[32:35], v[140:143], v[196:199], v[32:35]
	v_mfma_f32_16x16x32_bf16 v[28:31], v[148:151], v[196:199], v[28:31]
	v_mfma_f32_16x16x32_bf16 v[24:27], v[140:143], v[192:195], v[24:27]
	v_mfma_f32_16x16x32_bf16 v[20:23], v[148:151], v[192:195], v[20:23]
	v_mfma_f32_16x16x32_bf16 v[16:19], v[140:143], v[188:191], v[16:19]
	v_mfma_f32_16x16x32_bf16 v[12:15], v[148:151], v[188:191], v[12:15]
	v_mfma_f32_16x16x32_bf16 v[8:11], v[140:143], v[184:187], v[8:11]
	v_mfma_f32_16x16x32_bf16 v[4:7], v[148:151], v[184:187], v[4:7]
	s_setprio 0
.LBB0_1179:
	s_barrier
	v_add_u32_e32 v136, 0x18000, v224
	v_add_u32_e32 v148, 0x1c000, v224
	ds_read_b128 v[152:155], v136
	ds_read_b128 v[156:159], v136 offset:1024
	ds_read_b128 v[160:163], v136 offset:2048
	ds_read_b128 v[164:167], v136 offset:3072
	ds_read_b128 v[136:139], v148
	ds_read_b128 v[140:143], v148 offset:1024
	ds_read_b128 v[144:147], v148 offset:2048
	ds_read_b128 v[148:151], v148 offset:3072
	s_mov_b32 m0, s66
	s_waitcnt lgkmcnt(0)
	ds_read_b128 v[180:183], v225 offset:32768
	ds_read_b128 v[196:199], v225 offset:33792
	ds_read_b128 v[176:179], v225 offset:34816
	ds_read_b128 v[192:195], v225 offset:35840
	ds_read_b128 v[172:175], v225 offset:36864
	ds_read_b128 v[188:191], v225 offset:37888
	ds_read_b128 v[168:171], v225 offset:38912
	ds_read_b128 v[184:187], v225 offset:39936
	global_load_lds_dwordx4 v218, s[56:57]
	s_mov_b32 m0, s67
	s_nop 0
	global_load_lds_dwordx4 v220, s[56:57]
	s_waitcnt vmcnt(8)
	s_waitcnt lgkmcnt(0)
	s_barrier
	s_setprio 1
	s_waitcnt lgkmcnt(0)
	v_mfma_f32_16x16x32_bf16 v[132:135], v[152:155], v[180:183], v[132:135]
	v_mfma_f32_16x16x32_bf16 v[128:131], v[160:163], v[180:183], v[128:131]
	v_mfma_f32_16x16x32_bf16 v[124:127], v[152:155], v[176:179], v[124:127]
	v_mfma_f32_16x16x32_bf16 v[120:123], v[160:163], v[176:179], v[120:123]
	v_mfma_f32_16x16x32_bf16 v[116:119], v[152:155], v[172:175], v[116:119]
	v_mfma_f32_16x16x32_bf16 v[112:115], v[160:163], v[172:175], v[112:115]
	v_mfma_f32_16x16x32_bf16 v[108:111], v[152:155], v[168:171], v[108:111]
	v_mfma_f32_16x16x32_bf16 v[104:107], v[160:163], v[168:171], v[104:107]
	v_mfma_f32_16x16x32_bf16 v[132:135], v[156:159], v[196:199], v[132:135]
	v_mfma_f32_16x16x32_bf16 v[128:131], v[164:167], v[196:199], v[128:131]
	v_mfma_f32_16x16x32_bf16 v[124:127], v[156:159], v[192:195], v[124:127]
	v_mfma_f32_16x16x32_bf16 v[120:123], v[164:167], v[192:195], v[120:123]
	v_mfma_f32_16x16x32_bf16 v[116:119], v[156:159], v[188:191], v[116:119]
	v_mfma_f32_16x16x32_bf16 v[112:115], v[164:167], v[188:191], v[112:115]
	v_mfma_f32_16x16x32_bf16 v[108:111], v[156:159], v[184:187], v[108:111]
	v_mfma_f32_16x16x32_bf16 v[104:107], v[164:167], v[184:187], v[104:107]
	v_mfma_f32_16x16x32_bf16 v[100:103], v[136:139], v[180:183], v[100:103]
	v_mfma_f32_16x16x32_bf16 v[96:99], v[144:147], v[180:183], v[96:99]
	v_mfma_f32_16x16x32_bf16 v[92:95], v[136:139], v[176:179], v[92:95]
	v_mfma_f32_16x16x32_bf16 v[88:91], v[144:147], v[176:179], v[88:91]
	v_mfma_f32_16x16x32_bf16 v[80:83], v[136:139], v[172:175], v[80:83]
	v_mfma_f32_16x16x32_bf16 v[76:79], v[144:147], v[172:175], v[76:79]
	v_mfma_f32_16x16x32_bf16 v[72:75], v[136:139], v[168:171], v[72:75]
	v_mfma_f32_16x16x32_bf16 v[68:71], v[144:147], v[168:171], v[68:71]
	v_mfma_f32_16x16x32_bf16 v[100:103], v[140:143], v[196:199], v[100:103]
	v_mfma_f32_16x16x32_bf16 v[96:99], v[148:151], v[196:199], v[96:99]
	v_mfma_f32_16x16x32_bf16 v[92:95], v[140:143], v[192:195], v[92:95]
	v_mfma_f32_16x16x32_bf16 v[88:91], v[148:151], v[192:195], v[88:91]
	v_mfma_f32_16x16x32_bf16 v[80:83], v[140:143], v[188:191], v[80:83]
	v_mfma_f32_16x16x32_bf16 v[76:79], v[148:151], v[188:191], v[76:79]
	v_mfma_f32_16x16x32_bf16 v[72:75], v[140:143], v[184:187], v[72:75]
	v_mfma_f32_16x16x32_bf16 v[68:71], v[148:151], v[184:187], v[68:71]
	s_setprio 0
	s_barrier
	s_and_b64 vcc, exec, s[4:5]
	s_cbranch_vccnz .LBB0_1181
	ds_read_b128 v[180:183], v225 offset:49152
	ds_read_b128 v[196:199], v225 offset:50176
	ds_read_b128 v[176:179], v225 offset:51200
	ds_read_b128 v[192:195], v225 offset:52224
	ds_read_b128 v[172:175], v225 offset:53248
	ds_read_b128 v[188:191], v225 offset:54272
	ds_read_b128 v[168:171], v225 offset:55296
	ds_read_b128 v[184:187], v225 offset:56320
.LBB0_1181:
	v_mov_b32_e32 v213, v3
	v_lshl_add_u64 v[204:205], s[56:57], 0, v[2:3]
	v_lshl_add_u64 v[240:241], s[56:57], 0, v[212:213]
	s_add_u32 s56, s54, 0x8000
	s_addc_u32 s57, s55, 0
	s_mov_b32 m0, s69
	v_lshl_add_u64 v[242:243], s[56:57], 0, v[208:209]
	s_add_u32 s54, s54, 0xc000
	global_load_lds_dwordx4 v[242:243], off
	v_lshl_add_u64 v[242:243], s[56:57], 0, v[210:211]
	s_mov_b32 m0, s70
	s_addc_u32 s55, s55, 0
	global_load_lds_dwordx4 v[242:243], off
	v_lshl_add_u64 v[242:243], s[54:55], 0, v[208:209]
	s_mov_b32 m0, s73
	v_lshl_add_u64 v[204:205], v[204:205], 0, s[36:37]
	global_load_lds_dwordx4 v[242:243], off
	v_lshl_add_u64 v[242:243], s[54:55], 0, v[210:211]
	s_mov_b32 m0, s74
	s_and_b64 vcc, exec, s[4:5]
	global_load_lds_dwordx4 v[242:243], off
	s_mov_b32 m0, s71
	s_nop 0
	global_load_lds_dwordx4 v[204:205], off
	v_lshl_add_u64 v[204:205], v[240:241], 0, s[36:37]
	s_mov_b32 m0, s72
	s_nop 0
	global_load_lds_dwordx4 v[204:205], off
	s_waitcnt vmcnt(8)
	s_waitcnt lgkmcnt(0)
	s_barrier
	s_cbranch_vccnz .LBB0_1164
	s_setprio 1
	s_waitcnt lgkmcnt(0)
	v_mfma_f32_16x16x32_bf16 v[64:67], v[152:155], v[180:183], v[64:67]
	v_mfma_f32_16x16x32_bf16 v[60:63], v[160:163], v[180:183], v[60:63]
	v_mfma_f32_16x16x32_bf16 v[56:59], v[152:155], v[176:179], v[56:59]
	v_mfma_f32_16x16x32_bf16 v[52:55], v[160:163], v[176:179], v[52:55]
	v_mfma_f32_16x16x32_bf16 v[48:51], v[152:155], v[172:175], v[48:51]
	v_mfma_f32_16x16x32_bf16 v[44:47], v[160:163], v[172:175], v[44:47]
	v_mfma_f32_16x16x32_bf16 v[40:43], v[152:155], v[168:171], v[40:43]
	v_mfma_f32_16x16x32_bf16 v[36:39], v[160:163], v[168:171], v[36:39]
	v_mfma_f32_16x16x32_bf16 v[64:67], v[156:159], v[196:199], v[64:67]
	v_mfma_f32_16x16x32_bf16 v[60:63], v[164:167], v[196:199], v[60:63]
	v_mfma_f32_16x16x32_bf16 v[56:59], v[156:159], v[192:195], v[56:59]
	v_mfma_f32_16x16x32_bf16 v[52:55], v[164:167], v[192:195], v[52:55]
	v_mfma_f32_16x16x32_bf16 v[48:51], v[156:159], v[188:191], v[48:51]
	v_mfma_f32_16x16x32_bf16 v[44:47], v[164:167], v[188:191], v[44:47]
	v_mfma_f32_16x16x32_bf16 v[40:43], v[156:159], v[184:187], v[40:43]
	v_mfma_f32_16x16x32_bf16 v[36:39], v[164:167], v[184:187], v[36:39]
	v_mfma_f32_16x16x32_bf16 v[32:35], v[136:139], v[180:183], v[32:35]
	v_mfma_f32_16x16x32_bf16 v[28:31], v[144:147], v[180:183], v[28:31]
	v_mfma_f32_16x16x32_bf16 v[24:27], v[136:139], v[176:179], v[24:27]
	v_mfma_f32_16x16x32_bf16 v[20:23], v[144:147], v[176:179], v[20:23]
	v_mfma_f32_16x16x32_bf16 v[16:19], v[136:139], v[172:175], v[16:19]
	v_mfma_f32_16x16x32_bf16 v[12:15], v[144:147], v[172:175], v[12:15]
	v_mfma_f32_16x16x32_bf16 v[8:11], v[136:139], v[168:171], v[8:11]
	v_mfma_f32_16x16x32_bf16 v[4:7], v[144:147], v[168:171], v[4:7]
	v_mfma_f32_16x16x32_bf16 v[32:35], v[140:143], v[196:199], v[32:35]
	v_mfma_f32_16x16x32_bf16 v[28:31], v[148:151], v[196:199], v[28:31]
	v_mfma_f32_16x16x32_bf16 v[24:27], v[140:143], v[192:195], v[24:27]
	v_mfma_f32_16x16x32_bf16 v[20:23], v[148:151], v[192:195], v[20:23]
	v_mfma_f32_16x16x32_bf16 v[16:19], v[140:143], v[188:191], v[16:19]
	v_mfma_f32_16x16x32_bf16 v[12:15], v[148:151], v[188:191], v[12:15]
	v_mfma_f32_16x16x32_bf16 v[8:11], v[140:143], v[184:187], v[8:11]
	v_mfma_f32_16x16x32_bf16 v[4:7], v[148:151], v[184:187], v[4:7]
	s_setprio 0
	s_branch .LBB0_1164

.LBB0_1311:
	s_waitcnt vmcnt(8)
	s_waitcnt lgkmcnt(0)
	s_barrier
	s_setprio 1
	s_waitcnt lgkmcnt(0)
	v_mfma_f32_16x16x32_bf16 v[132:135], v[152:155], v[180:183], v[132:135]
	v_mfma_f32_16x16x32_bf16 v[128:131], v[160:163], v[180:183], v[128:131]
	v_mfma_f32_16x16x32_bf16 v[124:127], v[152:155], v[176:179], v[124:127]
	v_mfma_f32_16x16x32_bf16 v[120:123], v[160:163], v[176:179], v[120:123]
	v_mfma_f32_16x16x32_bf16 v[116:119], v[152:155], v[172:175], v[116:119]
	v_mfma_f32_16x16x32_bf16 v[112:115], v[160:163], v[172:175], v[112:115]
	v_mfma_f32_16x16x32_bf16 v[108:111], v[152:155], v[168:171], v[108:111]
	v_mfma_f32_16x16x32_bf16 v[104:107], v[160:163], v[168:171], v[104:107]
	v_mfma_f32_16x16x32_bf16 v[132:135], v[156:159], v[196:199], v[132:135]
	v_mfma_f32_16x16x32_bf16 v[128:131], v[164:167], v[196:199], v[128:131]
	v_mfma_f32_16x16x32_bf16 v[124:127], v[156:159], v[192:195], v[124:127]
	v_mfma_f32_16x16x32_bf16 v[120:123], v[164:167], v[192:195], v[120:123]
	v_mfma_f32_16x16x32_bf16 v[116:119], v[156:159], v[188:191], v[116:119]
	v_mfma_f32_16x16x32_bf16 v[112:115], v[164:167], v[188:191], v[112:115]
	v_mfma_f32_16x16x32_bf16 v[108:111], v[156:159], v[184:187], v[108:111]
	v_mfma_f32_16x16x32_bf16 v[104:107], v[164:167], v[184:187], v[104:107]
	v_mfma_f32_16x16x32_bf16 v[100:103], v[136:139], v[180:183], v[100:103]
	v_mfma_f32_16x16x32_bf16 v[96:99], v[144:147], v[180:183], v[96:99]
	v_mfma_f32_16x16x32_bf16 v[92:95], v[136:139], v[176:179], v[92:95]
	v_mfma_f32_16x16x32_bf16 v[88:91], v[144:147], v[176:179], v[88:91]
	v_mfma_f32_16x16x32_bf16 v[80:83], v[136:139], v[172:175], v[80:83]
	v_mfma_f32_16x16x32_bf16 v[76:79], v[144:147], v[172:175], v[76:79]
	v_mfma_f32_16x16x32_bf16 v[72:75], v[136:139], v[168:171], v[72:75]
	v_mfma_f32_16x16x32_bf16 v[68:71], v[144:147], v[168:171], v[68:71]
	v_mfma_f32_16x16x32_bf16 v[100:103], v[140:143], v[196:199], v[100:103]
	v_mfma_f32_16x16x32_bf16 v[96:99], v[148:151], v[196:199], v[96:99]
	v_mfma_f32_16x16x32_bf16 v[92:95], v[140:143], v[192:195], v[92:95]
	v_mfma_f32_16x16x32_bf16 v[88:91], v[148:151], v[192:195], v[88:91]
	v_mfma_f32_16x16x32_bf16 v[80:83], v[140:143], v[188:191], v[80:83]
	v_mfma_f32_16x16x32_bf16 v[76:79], v[148:151], v[188:191], v[76:79]
	v_mfma_f32_16x16x32_bf16 v[72:75], v[140:143], v[184:187], v[72:75]
	v_mfma_f32_16x16x32_bf16 v[68:71], v[148:151], v[184:187], v[68:71]
	s_setprio 0
	s_barrier
	v_cndmask_b32_e64 v200, 0, 1, s[2:3]
	v_cmp_ne_u32_e64 s[4:5], 1, v200
	s_andn2_b64 vcc, exec, s[2:3]
	s_cbranch_vccnz .LBB0_1313
	ds_read_b128 v[180:183], v242 offset:16384
	ds_read_b128 v[196:199], v242 offset:17408
	ds_read_b128 v[176:179], v242 offset:18432
	ds_read_b128 v[192:195], v242 offset:19456
	ds_read_b128 v[172:175], v242 offset:20480
	ds_read_b128 v[188:191], v242 offset:21504
	ds_read_b128 v[168:171], v242 offset:22528
	ds_read_b128 v[184:187], v242 offset:23552
.LBB0_1313:
	s_add_u32 s56, s52, 0x80
	s_addc_u32 s57, s53, 0
	s_and_b64 s[54:55], s[54:55], exec
	s_cselect_b32 s55, s41, s83
	s_cselect_b32 s54, s43, s82
	s_mov_b32 m0, s65
	s_cselect_b32 s57, s25, s57
	s_cselect_b32 s56, s24, s56
	v_lshl_add_u64 v[204:205], s[54:55], 0, v[208:209]
	s_add_u32 s86, s54, 0x4000
	global_load_lds_dwordx4 v[204:205], off
	v_lshl_add_u64 v[204:205], s[54:55], 0, v[210:211]
	s_mov_b32 m0, s66
	s_addc_u32 s87, s55, 0
	global_load_lds_dwordx4 v[204:205], off
	v_lshl_add_u64 v[204:205], s[86:87], 0, v[208:209]
	s_mov_b32 m0, s67
	s_and_b64 vcc, exec, s[4:5]
	global_load_lds_dwordx4 v[204:205], off
	v_lshl_add_u64 v[204:205], s[86:87], 0, v[210:211]
	s_mov_b32 m0, s68
	s_nop 0
	global_load_lds_dwordx4 v[204:205], off
	s_mov_b32 m0, s11
	s_nop 0
	global_load_lds_dwordx4 v2, s[56:57]
	s_mov_b32 m0, s69
	s_nop 0
	global_load_lds_dwordx4 v212, s[56:57]
	s_waitcnt vmcnt(8)
	s_waitcnt lgkmcnt(0)
	s_barrier
	s_cbranch_vccnz .LBB0_1315
	s_setprio 1
	s_waitcnt lgkmcnt(0)
	v_mfma_f32_16x16x32_bf16 v[64:67], v[152:155], v[180:183], v[64:67]
	v_mfma_f32_16x16x32_bf16 v[60:63], v[160:163], v[180:183], v[60:63]
	v_mfma_f32_16x16x32_bf16 v[56:59], v[152:155], v[176:179], v[56:59]
	v_mfma_f32_16x16x32_bf16 v[52:55], v[160:163], v[176:179], v[52:55]
	v_mfma_f32_16x16x32_bf16 v[48:51], v[152:155], v[172:175], v[48:51]
	v_mfma_f32_16x16x32_bf16 v[44:47], v[160:163], v[172:175], v[44:47]
	v_mfma_f32_16x16x32_bf16 v[40:43], v[152:155], v[168:171], v[40:43]
	v_mfma_f32_16x16x32_bf16 v[36:39], v[160:163], v[168:171], v[36:39]
	v_mfma_f32_16x16x32_bf16 v[64:67], v[156:159], v[196:199], v[64:67]
	v_mfma_f32_16x16x32_bf16 v[60:63], v[164:167], v[196:199], v[60:63]
	v_mfma_f32_16x16x32_bf16 v[56:59], v[156:159], v[192:195], v[56:59]
	v_mfma_f32_16x16x32_bf16 v[52:55], v[164:167], v[192:195], v[52:55]
	v_mfma_f32_16x16x32_bf16 v[48:51], v[156:159], v[188:191], v[48:51]
	v_mfma_f32_16x16x32_bf16 v[44:47], v[164:167], v[188:191], v[44:47]
	v_mfma_f32_16x16x32_bf16 v[40:43], v[156:159], v[184:187], v[40:43]
	v_mfma_f32_16x16x32_bf16 v[36:39], v[164:167], v[184:187], v[36:39]
	v_mfma_f32_16x16x32_bf16 v[32:35], v[136:139], v[180:183], v[32:35]
	v_mfma_f32_16x16x32_bf16 v[28:31], v[144:147], v[180:183], v[28:31]
	v_mfma_f32_16x16x32_bf16 v[24:27], v[136:139], v[176:179], v[24:27]
	v_mfma_f32_16x16x32_bf16 v[20:23], v[144:147], v[176:179], v[20:23]
	v_mfma_f32_16x16x32_bf16 v[16:19], v[136:139], v[172:175], v[16:19]
	v_mfma_f32_16x16x32_bf16 v[12:15], v[144:147], v[172:175], v[12:15]
	v_mfma_f32_16x16x32_bf16 v[8:11], v[136:139], v[168:171], v[8:11]
	v_mfma_f32_16x16x32_bf16 v[4:7], v[144:147], v[168:171], v[4:7]
	v_mfma_f32_16x16x32_bf16 v[32:35], v[140:143], v[196:199], v[32:35]
	v_mfma_f32_16x16x32_bf16 v[28:31], v[148:151], v[196:199], v[28:31]
	v_mfma_f32_16x16x32_bf16 v[24:27], v[140:143], v[192:195], v[24:27]
	v_mfma_f32_16x16x32_bf16 v[20:23], v[148:151], v[192:195], v[20:23]
	v_mfma_f32_16x16x32_bf16 v[16:19], v[140:143], v[188:191], v[16:19]
	v_mfma_f32_16x16x32_bf16 v[12:15], v[148:151], v[188:191], v[12:15]
	v_mfma_f32_16x16x32_bf16 v[8:11], v[140:143], v[184:187], v[8:11]
	v_mfma_f32_16x16x32_bf16 v[4:7], v[148:151], v[184:187], v[4:7]
	s_setprio 0
.LBB0_1315:
	s_barrier
	v_add_u32_e32 v136, 0x18000, v241
	v_add_u32_e32 v148, 0x1c000, v241
	ds_read_b128 v[152:155], v136
	ds_read_b128 v[156:159], v136 offset:1024
	ds_read_b128 v[160:163], v136 offset:2048
	ds_read_b128 v[164:167], v136 offset:3072
	ds_read_b128 v[136:139], v148
	ds_read_b128 v[140:143], v148 offset:1024
	ds_read_b128 v[144:147], v148 offset:2048
	ds_read_b128 v[148:151], v148 offset:3072
	s_mov_b32 m0, s70
	s_waitcnt lgkmcnt(0)
	ds_read_b128 v[180:183], v242 offset:32768
	ds_read_b128 v[196:199], v242 offset:33792
	ds_read_b128 v[176:179], v242 offset:34816
	ds_read_b128 v[192:195], v242 offset:35840
	ds_read_b128 v[172:175], v242 offset:36864
	ds_read_b128 v[188:191], v242 offset:37888
	ds_read_b128 v[168:171], v242 offset:38912
	ds_read_b128 v[184:187], v242 offset:39936
	global_load_lds_dwordx4 v218, s[56:57]
	s_mov_b32 m0, s71
	s_nop 0
	global_load_lds_dwordx4 v219, s[56:57]
	s_waitcnt vmcnt(8)
	s_waitcnt lgkmcnt(0)
	s_barrier
	s_setprio 1
	s_waitcnt lgkmcnt(0)
	v_mfma_f32_16x16x32_bf16 v[132:135], v[152:155], v[180:183], v[132:135]
	v_mfma_f32_16x16x32_bf16 v[128:131], v[160:163], v[180:183], v[128:131]
	v_mfma_f32_16x16x32_bf16 v[124:127], v[152:155], v[176:179], v[124:127]
	v_mfma_f32_16x16x32_bf16 v[120:123], v[160:163], v[176:179], v[120:123]
	v_mfma_f32_16x16x32_bf16 v[116:119], v[152:155], v[172:175], v[116:119]
	v_mfma_f32_16x16x32_bf16 v[112:115], v[160:163], v[172:175], v[112:115]
	v_mfma_f32_16x16x32_bf16 v[108:111], v[152:155], v[168:171], v[108:111]
	v_mfma_f32_16x16x32_bf16 v[104:107], v[160:163], v[168:171], v[104:107]
	v_mfma_f32_16x16x32_bf16 v[132:135], v[156:159], v[196:199], v[132:135]
	v_mfma_f32_16x16x32_bf16 v[128:131], v[164:167], v[196:199], v[128:131]
	v_mfma_f32_16x16x32_bf16 v[124:127], v[156:159], v[192:195], v[124:127]
	v_mfma_f32_16x16x32_bf16 v[120:123], v[164:167], v[192:195], v[120:123]
	v_mfma_f32_16x16x32_bf16 v[116:119], v[156:159], v[188:191], v[116:119]
	v_mfma_f32_16x16x32_bf16 v[112:115], v[164:167], v[188:191], v[112:115]
	v_mfma_f32_16x16x32_bf16 v[108:111], v[156:159], v[184:187], v[108:111]
	v_mfma_f32_16x16x32_bf16 v[104:107], v[164:167], v[184:187], v[104:107]
	v_mfma_f32_16x16x32_bf16 v[100:103], v[136:139], v[180:183], v[100:103]
	v_mfma_f32_16x16x32_bf16 v[96:99], v[144:147], v[180:183], v[96:99]
	v_mfma_f32_16x16x32_bf16 v[92:95], v[136:139], v[176:179], v[92:95]
	v_mfma_f32_16x16x32_bf16 v[88:91], v[144:147], v[176:179], v[88:91]
	v_mfma_f32_16x16x32_bf16 v[80:83], v[136:139], v[172:175], v[80:83]
	v_mfma_f32_16x16x32_bf16 v[76:79], v[144:147], v[172:175], v[76:79]
	v_mfma_f32_16x16x32_bf16 v[72:75], v[136:139], v[168:171], v[72:75]
	v_mfma_f32_16x16x32_bf16 v[68:71], v[144:147], v[168:171], v[68:71]
	v_mfma_f32_16x16x32_bf16 v[100:103], v[140:143], v[196:199], v[100:103]
	v_mfma_f32_16x16x32_bf16 v[96:99], v[148:151], v[196:199], v[96:99]
	v_mfma_f32_16x16x32_bf16 v[92:95], v[140:143], v[192:195], v[92:95]
	v_mfma_f32_16x16x32_bf16 v[88:91], v[148:151], v[192:195], v[88:91]
	v_mfma_f32_16x16x32_bf16 v[80:83], v[140:143], v[188:191], v[80:83]
	v_mfma_f32_16x16x32_bf16 v[76:79], v[148:151], v[188:191], v[76:79]
	v_mfma_f32_16x16x32_bf16 v[72:75], v[140:143], v[184:187], v[72:75]
	v_mfma_f32_16x16x32_bf16 v[68:71], v[148:151], v[184:187], v[68:71]
	s_setprio 0
	s_barrier
	s_and_b64 vcc, exec, s[4:5]
	s_cbranch_vccnz .LBB0_1317
	ds_read_b128 v[180:183], v242 offset:49152
	ds_read_b128 v[196:199], v242 offset:50176
	ds_read_b128 v[176:179], v242 offset:51200
	ds_read_b128 v[192:195], v242 offset:52224
	ds_read_b128 v[172:175], v242 offset:53248
	ds_read_b128 v[188:191], v242 offset:54272
	ds_read_b128 v[168:171], v242 offset:55296
	ds_read_b128 v[184:187], v242 offset:56320
.LBB0_1317:
	v_mov_b32_e32 v213, v3
	v_lshl_add_u64 v[204:205], s[56:57], 0, v[2:3]
	v_lshl_add_u64 v[206:207], s[56:57], 0, v[212:213]
	s_add_u32 s56, s54, 0x8000
	s_addc_u32 s57, s55, 0
	s_mov_b32 m0, s72
	v_lshl_add_u64 v[200:201], s[56:57], 0, v[208:209]
	s_add_u32 s54, s54, 0xc000
	global_load_lds_dwordx4 v[200:201], off
	v_lshl_add_u64 v[200:201], s[56:57], 0, v[210:211]
	s_mov_b32 m0, s73
	s_addc_u32 s55, s55, 0
	global_load_lds_dwordx4 v[200:201], off
	v_lshl_add_u64 v[200:201], s[54:55], 0, v[208:209]
	s_mov_b32 m0, s76
	s_and_b64 vcc, exec, s[4:5]
	global_load_lds_dwordx4 v[200:201], off
	v_lshl_add_u64 v[200:201], s[54:55], 0, v[210:211]
	s_mov_b32 m0, s77
	s_nop 0
	global_load_lds_dwordx4 v[200:201], off
	v_lshl_add_u64 v[200:201], v[204:205], 0, s[36:37]
	s_mov_b32 m0, s74
	s_nop 0
	global_load_lds_dwordx4 v[200:201], off
	v_lshl_add_u64 v[200:201], v[206:207], 0, s[36:37]
	s_mov_b32 m0, s75
	s_nop 0
	global_load_lds_dwordx4 v[200:201], off
	s_waitcnt vmcnt(8)
	s_waitcnt lgkmcnt(0)
	s_barrier
	s_cbranch_vccnz .LBB0_1308
	s_setprio 1
	s_waitcnt lgkmcnt(0)
	v_mfma_f32_16x16x32_bf16 v[64:67], v[152:155], v[180:183], v[64:67]
	v_mfma_f32_16x16x32_bf16 v[60:63], v[160:163], v[180:183], v[60:63]
	v_mfma_f32_16x16x32_bf16 v[56:59], v[152:155], v[176:179], v[56:59]
	v_mfma_f32_16x16x32_bf16 v[52:55], v[160:163], v[176:179], v[52:55]
	v_mfma_f32_16x16x32_bf16 v[48:51], v[152:155], v[172:175], v[48:51]
	v_mfma_f32_16x16x32_bf16 v[44:47], v[160:163], v[172:175], v[44:47]
	v_mfma_f32_16x16x32_bf16 v[40:43], v[152:155], v[168:171], v[40:43]
	v_mfma_f32_16x16x32_bf16 v[36:39], v[160:163], v[168:171], v[36:39]
	v_mfma_f32_16x16x32_bf16 v[64:67], v[156:159], v[196:199], v[64:67]
	v_mfma_f32_16x16x32_bf16 v[60:63], v[164:167], v[196:199], v[60:63]
	v_mfma_f32_16x16x32_bf16 v[56:59], v[156:159], v[192:195], v[56:59]
	v_mfma_f32_16x16x32_bf16 v[52:55], v[164:167], v[192:195], v[52:55]
	v_mfma_f32_16x16x32_bf16 v[48:51], v[156:159], v[188:191], v[48:51]
	v_mfma_f32_16x16x32_bf16 v[44:47], v[164:167], v[188:191], v[44:47]
	v_mfma_f32_16x16x32_bf16 v[40:43], v[156:159], v[184:187], v[40:43]
	v_mfma_f32_16x16x32_bf16 v[36:39], v[164:167], v[184:187], v[36:39]
	v_mfma_f32_16x16x32_bf16 v[32:35], v[136:139], v[180:183], v[32:35]
	v_mfma_f32_16x16x32_bf16 v[28:31], v[144:147], v[180:183], v[28:31]
	v_mfma_f32_16x16x32_bf16 v[24:27], v[136:139], v[176:179], v[24:27]
	v_mfma_f32_16x16x32_bf16 v[20:23], v[144:147], v[176:179], v[20:23]
	v_mfma_f32_16x16x32_bf16 v[16:19], v[136:139], v[172:175], v[16:19]
	v_mfma_f32_16x16x32_bf16 v[12:15], v[144:147], v[172:175], v[12:15]
	v_mfma_f32_16x16x32_bf16 v[8:11], v[136:139], v[168:171], v[8:11]
	v_mfma_f32_16x16x32_bf16 v[4:7], v[144:147], v[168:171], v[4:7]
	v_mfma_f32_16x16x32_bf16 v[32:35], v[140:143], v[196:199], v[32:35]
	v_mfma_f32_16x16x32_bf16 v[28:31], v[148:151], v[196:199], v[28:31]
	v_mfma_f32_16x16x32_bf16 v[24:27], v[140:143], v[192:195], v[24:27]
	v_mfma_f32_16x16x32_bf16 v[20:23], v[148:151], v[192:195], v[20:23]
	v_mfma_f32_16x16x32_bf16 v[16:19], v[140:143], v[188:191], v[16:19]
	v_mfma_f32_16x16x32_bf16 v[12:15], v[148:151], v[188:191], v[12:15]
	v_mfma_f32_16x16x32_bf16 v[8:11], v[140:143], v[184:187], v[8:11]
	v_mfma_f32_16x16x32_bf16 v[4:7], v[148:151], v[184:187], v[4:7]
	s_setprio 0
	s_branch .LBB0_1308

.LBB0_1429:
	s_add_u32 s52, s48, 0x80
	s_addc_u32 s53, s49, 0
	s_and_b64 s[50:51], s[50:51], exec
	s_cselect_b32 s51, s15, s74
	s_cselect_b32 s50, s39, s73
	s_mov_b32 m0, s55
	s_cselect_b32 s53, s25, s53
	s_cselect_b32 s52, s24, s52
	v_lshl_add_u64 v[200:201], s[50:51], 0, v[208:209]
	s_add_u32 s76, s50, 0x4000
	global_load_lds_dwordx4 v[200:201], off
	v_lshl_add_u64 v[200:201], s[50:51], 0, v[210:211]
	s_mov_b32 m0, s56
	s_addc_u32 s77, s51, 0
	global_load_lds_dwordx4 v[200:201], off
	v_lshl_add_u64 v[200:201], s[76:77], 0, v[208:209]
	s_mov_b32 m0, s57
	s_and_b64 vcc, exec, s[4:5]
	global_load_lds_dwordx4 v[200:201], off
	v_lshl_add_u64 v[200:201], s[76:77], 0, v[210:211]
	s_mov_b32 m0, s59
	s_nop 0
	global_load_lds_dwordx4 v[200:201], off
	s_mov_b32 m0, s7
	s_nop 0
	global_load_lds_dwordx4 v2, s[52:53]
	s_mov_b32 m0, s60
	s_nop 0
	global_load_lds_dwordx4 v212, s[52:53]
	s_waitcnt vmcnt(8)
	s_waitcnt lgkmcnt(0)
	s_barrier
	s_cbranch_vccnz .LBB0_1431
	s_setprio 1
	s_waitcnt lgkmcnt(0)
	v_mfma_f32_16x16x32_bf16 v[64:67], v[152:155], v[180:183], v[64:67]
	v_mfma_f32_16x16x32_bf16 v[60:63], v[160:163], v[180:183], v[60:63]
	v_mfma_f32_16x16x32_bf16 v[56:59], v[152:155], v[176:179], v[56:59]
	v_mfma_f32_16x16x32_bf16 v[52:55], v[160:163], v[176:179], v[52:55]
	v_mfma_f32_16x16x32_bf16 v[48:51], v[152:155], v[172:175], v[48:51]
	v_mfma_f32_16x16x32_bf16 v[44:47], v[160:163], v[172:175], v[44:47]
	v_mfma_f32_16x16x32_bf16 v[40:43], v[152:155], v[168:171], v[40:43]
	v_mfma_f32_16x16x32_bf16 v[36:39], v[160:163], v[168:171], v[36:39]
	v_mfma_f32_16x16x32_bf16 v[64:67], v[156:159], v[196:199], v[64:67]
	v_mfma_f32_16x16x32_bf16 v[60:63], v[164:167], v[196:199], v[60:63]
	v_mfma_f32_16x16x32_bf16 v[56:59], v[156:159], v[192:195], v[56:59]
	v_mfma_f32_16x16x32_bf16 v[52:55], v[164:167], v[192:195], v[52:55]
	v_mfma_f32_16x16x32_bf16 v[48:51], v[156:159], v[188:191], v[48:51]
	v_mfma_f32_16x16x32_bf16 v[44:47], v[164:167], v[188:191], v[44:47]
	v_mfma_f32_16x16x32_bf16 v[40:43], v[156:159], v[184:187], v[40:43]
	v_mfma_f32_16x16x32_bf16 v[36:39], v[164:167], v[184:187], v[36:39]
	v_mfma_f32_16x16x32_bf16 v[32:35], v[136:139], v[180:183], v[32:35]
	v_mfma_f32_16x16x32_bf16 v[28:31], v[144:147], v[180:183], v[28:31]
	v_mfma_f32_16x16x32_bf16 v[24:27], v[136:139], v[176:179], v[24:27]
	v_mfma_f32_16x16x32_bf16 v[20:23], v[144:147], v[176:179], v[20:23]
	v_mfma_f32_16x16x32_bf16 v[16:19], v[136:139], v[172:175], v[16:19]
	v_mfma_f32_16x16x32_bf16 v[12:15], v[144:147], v[172:175], v[12:15]
	v_mfma_f32_16x16x32_bf16 v[8:11], v[136:139], v[168:171], v[8:11]
	v_mfma_f32_16x16x32_bf16 v[4:7], v[144:147], v[168:171], v[4:7]
	v_mfma_f32_16x16x32_bf16 v[32:35], v[140:143], v[196:199], v[32:35]
	v_mfma_f32_16x16x32_bf16 v[28:31], v[148:151], v[196:199], v[28:31]
	v_mfma_f32_16x16x32_bf16 v[24:27], v[140:143], v[192:195], v[24:27]
	v_mfma_f32_16x16x32_bf16 v[20:23], v[148:151], v[192:195], v[20:23]
	v_mfma_f32_16x16x32_bf16 v[16:19], v[140:143], v[188:191], v[16:19]
	v_mfma_f32_16x16x32_bf16 v[12:15], v[148:151], v[188:191], v[12:15]
	v_mfma_f32_16x16x32_bf16 v[8:11], v[140:143], v[184:187], v[8:11]
	v_mfma_f32_16x16x32_bf16 v[4:7], v[148:151], v[184:187], v[4:7]
	s_setprio 0
.LBB0_1431:
	s_barrier
	v_add_u32_e32 v136, 0x18000, v241
	v_add_u32_e32 v148, 0x1c000, v241
	ds_read_b128 v[152:155], v136
	ds_read_b128 v[156:159], v136 offset:1024
	ds_read_b128 v[160:163], v136 offset:2048
	ds_read_b128 v[164:167], v136 offset:3072
	ds_read_b128 v[136:139], v148
	ds_read_b128 v[140:143], v148 offset:1024
	ds_read_b128 v[144:147], v148 offset:2048
	ds_read_b128 v[148:151], v148 offset:3072
	s_mov_b32 m0, s61
	s_waitcnt lgkmcnt(0)
	ds_read_b128 v[180:183], v242 offset:32768
	ds_read_b128 v[196:199], v242 offset:33792
	ds_read_b128 v[176:179], v242 offset:34816
	ds_read_b128 v[192:195], v242 offset:35840
	ds_read_b128 v[172:175], v242 offset:36864
	ds_read_b128 v[188:191], v242 offset:37888
	ds_read_b128 v[168:171], v242 offset:38912
	ds_read_b128 v[184:187], v242 offset:39936
	global_load_lds_dwordx4 v218, s[52:53]
	s_mov_b32 m0, s62
	s_nop 0
	global_load_lds_dwordx4 v219, s[52:53]
	s_waitcnt vmcnt(8)
	s_waitcnt lgkmcnt(0)
	s_barrier
	s_setprio 1
	s_waitcnt lgkmcnt(0)
	v_mfma_f32_16x16x32_bf16 v[132:135], v[152:155], v[180:183], v[132:135]
	v_mfma_f32_16x16x32_bf16 v[128:131], v[160:163], v[180:183], v[128:131]
	v_mfma_f32_16x16x32_bf16 v[124:127], v[152:155], v[176:179], v[124:127]
	v_mfma_f32_16x16x32_bf16 v[120:123], v[160:163], v[176:179], v[120:123]
	v_mfma_f32_16x16x32_bf16 v[116:119], v[152:155], v[172:175], v[116:119]
	v_mfma_f32_16x16x32_bf16 v[112:115], v[160:163], v[172:175], v[112:115]
	v_mfma_f32_16x16x32_bf16 v[108:111], v[152:155], v[168:171], v[108:111]
	v_mfma_f32_16x16x32_bf16 v[104:107], v[160:163], v[168:171], v[104:107]
	v_mfma_f32_16x16x32_bf16 v[132:135], v[156:159], v[196:199], v[132:135]
	v_mfma_f32_16x16x32_bf16 v[128:131], v[164:167], v[196:199], v[128:131]
	v_mfma_f32_16x16x32_bf16 v[124:127], v[156:159], v[192:195], v[124:127]
	v_mfma_f32_16x16x32_bf16 v[120:123], v[164:167], v[192:195], v[120:123]
	v_mfma_f32_16x16x32_bf16 v[116:119], v[156:159], v[188:191], v[116:119]
	v_mfma_f32_16x16x32_bf16 v[112:115], v[164:167], v[188:191], v[112:115]
	v_mfma_f32_16x16x32_bf16 v[108:111], v[156:159], v[184:187], v[108:111]
	v_mfma_f32_16x16x32_bf16 v[104:107], v[164:167], v[184:187], v[104:107]
	v_mfma_f32_16x16x32_bf16 v[100:103], v[136:139], v[180:183], v[100:103]
	v_mfma_f32_16x16x32_bf16 v[96:99], v[144:147], v[180:183], v[96:99]
	v_mfma_f32_16x16x32_bf16 v[92:95], v[136:139], v[176:179], v[92:95]
	v_mfma_f32_16x16x32_bf16 v[88:91], v[144:147], v[176:179], v[88:91]
	v_mfma_f32_16x16x32_bf16 v[80:83], v[136:139], v[172:175], v[80:83]
	v_mfma_f32_16x16x32_bf16 v[76:79], v[144:147], v[172:175], v[76:79]
	v_mfma_f32_16x16x32_bf16 v[72:75], v[136:139], v[168:171], v[72:75]
	v_mfma_f32_16x16x32_bf16 v[68:71], v[144:147], v[168:171], v[68:71]
	v_mfma_f32_16x16x32_bf16 v[100:103], v[140:143], v[196:199], v[100:103]
	v_mfma_f32_16x16x32_bf16 v[96:99], v[148:151], v[196:199], v[96:99]
	v_mfma_f32_16x16x32_bf16 v[92:95], v[140:143], v[192:195], v[92:95]
	v_mfma_f32_16x16x32_bf16 v[88:91], v[148:151], v[192:195], v[88:91]
	v_mfma_f32_16x16x32_bf16 v[80:83], v[140:143], v[188:191], v[80:83]
	v_mfma_f32_16x16x32_bf16 v[76:79], v[148:151], v[188:191], v[76:79]
	v_mfma_f32_16x16x32_bf16 v[72:75], v[140:143], v[184:187], v[72:75]
	v_mfma_f32_16x16x32_bf16 v[68:71], v[148:151], v[184:187], v[68:71]
	s_setprio 0
	s_barrier
	s_and_b64 vcc, exec, s[4:5]
	s_cbranch_vccnz .LBB0_1433
	ds_read_b128 v[180:183], v242 offset:49152
	ds_read_b128 v[196:199], v242 offset:50176
	ds_read_b128 v[176:179], v242 offset:51200
	ds_read_b128 v[192:195], v242 offset:52224
	ds_read_b128 v[172:175], v242 offset:53248
	ds_read_b128 v[188:191], v242 offset:54272
	ds_read_b128 v[168:171], v242 offset:55296
	ds_read_b128 v[184:187], v242 offset:56320
.LBB0_1433:
	v_mov_b32_e32 v213, v3
	v_lshl_add_u64 v[200:201], s[52:53], 0, v[2:3]
	v_lshl_add_u64 v[204:205], s[52:53], 0, v[212:213]
	s_add_u32 s52, s50, 0x8000
	s_addc_u32 s53, s51, 0
	s_mov_b32 m0, s63
	v_lshl_add_u64 v[206:207], s[52:53], 0, v[208:209]
	s_add_u32 s50, s50, 0xc000
	global_load_lds_dwordx4 v[206:207], off
	v_lshl_add_u64 v[206:207], s[52:53], 0, v[210:211]
	s_mov_b32 m0, s64
	s_addc_u32 s51, s51, 0
	global_load_lds_dwordx4 v[206:207], off
	v_lshl_add_u64 v[206:207], s[50:51], 0, v[208:209]
	s_mov_b32 m0, s67
	v_lshl_add_u64 v[200:201], v[200:201], 0, s[36:37]
	global_load_lds_dwordx4 v[206:207], off
	v_lshl_add_u64 v[206:207], s[50:51], 0, v[210:211]
	s_mov_b32 m0, s68
	s_and_b64 vcc, exec, s[4:5]
	global_load_lds_dwordx4 v[206:207], off
	s_mov_b32 m0, s65
	s_nop 0
	global_load_lds_dwordx4 v[200:201], off
	v_lshl_add_u64 v[200:201], v[204:205], 0, s[36:37]
	s_mov_b32 m0, s66
	s_nop 0
	global_load_lds_dwordx4 v[200:201], off
	s_waitcnt vmcnt(8)
	s_waitcnt lgkmcnt(0)
	s_barrier
	s_cbranch_vccnz .LBB0_1424
	s_setprio 1
	s_waitcnt lgkmcnt(0)
	v_mfma_f32_16x16x32_bf16 v[64:67], v[152:155], v[180:183], v[64:67]
	v_mfma_f32_16x16x32_bf16 v[60:63], v[160:163], v[180:183], v[60:63]
	v_mfma_f32_16x16x32_bf16 v[56:59], v[152:155], v[176:179], v[56:59]
	v_mfma_f32_16x16x32_bf16 v[52:55], v[160:163], v[176:179], v[52:55]
	v_mfma_f32_16x16x32_bf16 v[48:51], v[152:155], v[172:175], v[48:51]
	v_mfma_f32_16x16x32_bf16 v[44:47], v[160:163], v[172:175], v[44:47]
	v_mfma_f32_16x16x32_bf16 v[40:43], v[152:155], v[168:171], v[40:43]
	v_mfma_f32_16x16x32_bf16 v[36:39], v[160:163], v[168:171], v[36:39]
	v_mfma_f32_16x16x32_bf16 v[64:67], v[156:159], v[196:199], v[64:67]
	v_mfma_f32_16x16x32_bf16 v[60:63], v[164:167], v[196:199], v[60:63]
	v_mfma_f32_16x16x32_bf16 v[56:59], v[156:159], v[192:195], v[56:59]
	v_mfma_f32_16x16x32_bf16 v[52:55], v[164:167], v[192:195], v[52:55]
	v_mfma_f32_16x16x32_bf16 v[48:51], v[156:159], v[188:191], v[48:51]
	v_mfma_f32_16x16x32_bf16 v[44:47], v[164:167], v[188:191], v[44:47]
	v_mfma_f32_16x16x32_bf16 v[40:43], v[156:159], v[184:187], v[40:43]
	v_mfma_f32_16x16x32_bf16 v[36:39], v[164:167], v[184:187], v[36:39]
	v_mfma_f32_16x16x32_bf16 v[32:35], v[136:139], v[180:183], v[32:35]
	v_mfma_f32_16x16x32_bf16 v[28:31], v[144:147], v[180:183], v[28:31]
	v_mfma_f32_16x16x32_bf16 v[24:27], v[136:139], v[176:179], v[24:27]
	v_mfma_f32_16x16x32_bf16 v[20:23], v[144:147], v[176:179], v[20:23]
	v_mfma_f32_16x16x32_bf16 v[16:19], v[136:139], v[172:175], v[16:19]
	v_mfma_f32_16x16x32_bf16 v[12:15], v[144:147], v[172:175], v[12:15]
	v_mfma_f32_16x16x32_bf16 v[8:11], v[136:139], v[168:171], v[8:11]
	v_mfma_f32_16x16x32_bf16 v[4:7], v[144:147], v[168:171], v[4:7]
	v_mfma_f32_16x16x32_bf16 v[32:35], v[140:143], v[196:199], v[32:35]
	v_mfma_f32_16x16x32_bf16 v[28:31], v[148:151], v[196:199], v[28:31]
	v_mfma_f32_16x16x32_bf16 v[24:27], v[140:143], v[192:195], v[24:27]
	v_mfma_f32_16x16x32_bf16 v[20:23], v[148:151], v[192:195], v[20:23]
	v_mfma_f32_16x16x32_bf16 v[16:19], v[140:143], v[188:191], v[16:19]
	v_mfma_f32_16x16x32_bf16 v[12:15], v[148:151], v[188:191], v[12:15]
	v_mfma_f32_16x16x32_bf16 v[8:11], v[140:143], v[184:187], v[8:11]
	v_mfma_f32_16x16x32_bf16 v[4:7], v[148:151], v[184:187], v[4:7]
	s_setprio 0
	s_branch .LBB0_1424
